# speedup vs baseline: 1.0101x; 1.0101x over previous
_Z4k_lnPKDF16_PKfS2_PfPDF16_Phi:
	s_load_dword s3, s[0:1], 0x30
	s_and_b32 s4, s2, 7
	s_lshr_b32 s2, s2, 3
	v_lshrrev_b32_e32 v1, 6, v0
	s_waitcnt lgkmcnt(0)
	s_ashr_i32 s5, s3, 31
	s_lshr_b32 s5, s5, 27
	s_add_i32 s5, s3, s5
	s_ashr_i32 s5, s5, 5
	s_mul_i32 s4, s5, s4
	s_add_i32 s4, s4, s2
	v_lshl_or_b32 v2, s4, 2, v1
	v_cmp_gt_i32_e32 vcc, s3, v2
	s_and_saveexec_b64 s[2:3], vcc
	s_cbranch_execz .LBB1_13
	s_load_dwordx8 s[4:11], s[0:1], 0x0
	v_ashrrev_i32_e32 v3, 31, v2
	v_lshlrev_b32_e32 v4, 3, v0
	v_lshlrev_b64 v[0:1], 11, v[2:3]
	v_and_b32_e32 v8, 0x1f8, v4
	s_waitcnt lgkmcnt(0)
	v_lshl_add_u64 v[0:1], s[4:5], 0, v[0:1]
	v_mov_b32_e32 v11, 0
	v_lshlrev_b32_e32 v10, 1, v8
	v_lshl_add_u64 v[0:1], v[0:1], 0, v[10:11]
	global_load_dwordx4 v[4:7], v[0:1], off offset:1024 nt
	global_load_dwordx4 v[12:15], v[0:1], off nt
	v_mbcnt_lo_u32_b32 v0, -1, 0
	v_mbcnt_hi_u32_b32 v9, -1, v0
	v_and_b32_e32 v0, 64, v9
	v_xor_b32_e32 v1, 32, v9
	v_add_u32_e32 v22, 64, v0
	v_cmp_lt_i32_e32 vcc, v1, v22
	v_xor_b32_e32 v10, 16, v9
	s_load_dwordx2 s[4:5], s[0:1], 0x20
	v_cndmask_b32_e32 v0, v9, v1, vcc
	v_lshlrev_b32_e32 v54, 2, v0
	v_cmp_lt_i32_e32 vcc, v10, v22
	s_cmp_lg_u64 s[10:11], 0
	s_cselect_b64 s[2:3], -1, 0
	s_cmp_eq_u64 s[10:11], 0
	s_waitcnt vmcnt(1)
	v_cvt_f32_f16_e32 v20, v4
	s_waitcnt vmcnt(0)
	v_cvt_f32_f16_e32 v28, v14
	v_cvt_f32_f16_sdwa v29, v14 dst_sel:DWORD dst_unused:UNUSED_PAD src0_sel:WORD_1
	v_cvt_f32_f16_e32 v14, v12
	v_cvt_f32_f16_e32 v26, v15
	v_cvt_f32_f16_sdwa v27, v15 dst_sel:DWORD dst_unused:UNUSED_PAD src0_sel:WORD_1
	v_cvt_f32_f16_sdwa v15, v12 dst_sel:DWORD dst_unused:UNUSED_PAD src0_sel:WORD_1
	v_cvt_f32_f16_e32 v12, v13
	v_cvt_f32_f16_sdwa v13, v13 dst_sel:DWORD dst_unused:UNUSED_PAD src0_sel:WORD_1
	v_cvt_f32_f16_sdwa v21, v4 dst_sel:DWORD dst_unused:UNUSED_PAD src0_sel:WORD_1
	v_add_f32_e32 v4, 0, v14
	v_add_f32_e32 v4, v4, v15
	v_add_f32_e32 v4, v4, v12
	v_add_f32_e32 v4, v4, v13
	v_add_f32_e32 v4, v4, v28
	v_add_f32_e32 v4, v4, v29
	v_cvt_f32_f16_e32 v18, v5
	v_add_f32_e32 v4, v4, v26
	v_cvt_f32_f16_sdwa v19, v5 dst_sel:DWORD dst_unused:UNUSED_PAD src0_sel:WORD_1
	v_add_f32_e32 v4, v4, v27
	v_cvt_f32_f16_e32 v16, v6
	v_add_f32_e32 v4, v4, v20
	v_cvt_f32_f16_sdwa v17, v6 dst_sel:DWORD dst_unused:UNUSED_PAD src0_sel:WORD_1
	v_add_f32_e32 v4, v4, v21
	v_cvt_f32_f16_e32 v0, v7
	v_add_f32_e32 v4, v4, v18
	v_cvt_f32_f16_sdwa v1, v7 dst_sel:DWORD dst_unused:UNUSED_PAD src0_sel:WORD_1
	v_add_f32_e32 v4, v4, v19
	v_add_f32_e32 v4, v4, v16
	v_add_f32_e32 v4, v4, v17
	v_add_f32_e32 v4, v4, v0
	v_add_f32_e32 v4, v4, v1
	ds_bpermute_b32 v5, v54, v4
	v_cndmask_b32_e32 v7, v9, v10, vcc
	v_lshlrev_b32_e32 v55, 2, v7
	v_xor_b32_e32 v6, 8, v9
	v_cmp_lt_i32_e32 vcc, v6, v22
	s_waitcnt lgkmcnt(0)
	v_add_f32_e32 v4, v4, v5
	ds_bpermute_b32 v5, v55, v4
	v_cndmask_b32_e32 v6, v9, v6, vcc
	v_lshlrev_b32_e32 v56, 2, v6
	v_xor_b32_e32 v7, 4, v9
	v_cmp_lt_i32_e32 vcc, v7, v22
	s_waitcnt lgkmcnt(0)
	v_add_f32_e32 v4, v4, v5
	ds_bpermute_b32 v5, v56, v4
	v_cndmask_b32_e32 v7, v9, v7, vcc
	v_lshlrev_b32_e32 v57, 2, v7
	v_xor_b32_e32 v6, 2, v9
	v_cmp_lt_i32_e32 vcc, v6, v22
	s_waitcnt lgkmcnt(0)
	v_add_f32_e32 v4, v4, v5
	ds_bpermute_b32 v5, v57, v4
	v_cndmask_b32_e32 v6, v9, v6, vcc
	v_lshlrev_b32_e32 v58, 2, v6
	v_xor_b32_e32 v7, 1, v9
	v_cmp_lt_i32_e32 vcc, v7, v22
	s_waitcnt lgkmcnt(0)
	v_add_f32_e32 v4, v4, v5
	ds_bpermute_b32 v5, v58, v4
	v_cndmask_b32_e32 v6, v9, v7, vcc
	v_lshlrev_b32_e32 v10, 2, v8
	v_lshlrev_b32_e32 v9, 2, v6
	s_waitcnt lgkmcnt(0)
	v_add_f32_e32 v30, v4, v5
	global_load_dwordx4 v[4:7], v10, s[6:7]
	global_load_dwordx4 v[22:25], v10, s[8:9]
	global_load_dwordx4 v[32:35], v10, s[6:7] offset:16
	global_load_dwordx4 v[36:39], v10, s[8:9] offset:16
	ds_bpermute_b32 v31, v9, v30
	s_waitcnt lgkmcnt(0)
	v_add_f32_e32 v30, v30, v31
	v_mul_f32_e32 v30, 0x3a800000, v30
	v_pk_add_f32 v[40:41], v[14:15], v[30:31] op_sel_hi:[1,0] neg_lo:[0,1] neg_hi:[0,1]
	v_pk_add_f32 v[42:43], v[12:13], v[30:31] op_sel_hi:[1,0] neg_lo:[0,1] neg_hi:[0,1]
	v_pk_add_f32 v[12:13], v[18:19], v[30:31] op_sel_hi:[1,0] neg_lo:[0,1] neg_hi:[0,1]
	v_pk_add_f32 v[18:19], v[16:17], v[30:31] op_sel_hi:[1,0] neg_lo:[0,1] neg_hi:[0,1]
	v_pk_add_f32 v[16:17], v[0:1], v[30:31] op_sel_hi:[1,0] neg_lo:[0,1] neg_hi:[0,1]
	v_pk_mul_f32 v[0:1], v[40:41], v[40:41]
	v_pk_add_f32 v[14:15], v[20:21], v[30:31] op_sel_hi:[1,0] neg_lo:[0,1] neg_hi:[0,1]
	v_pk_mul_f32 v[20:21], v[42:43], v[42:43]
	v_add_f32_e32 v0, v0, v1
	v_pk_add_f32 v[44:45], v[28:29], v[30:31] op_sel_hi:[1,0] neg_lo:[0,1] neg_hi:[0,1]
	v_add_f32_e32 v0, v0, v20
	v_pk_mul_f32 v[28:29], v[44:45], v[44:45]
	v_add_f32_e32 v0, v0, v21
	v_pk_add_f32 v[26:27], v[26:27], v[30:31] op_sel_hi:[1,0] neg_lo:[0,1] neg_hi:[0,1]
	v_add_f32_e32 v0, v0, v28
	v_pk_mul_f32 v[30:31], v[26:27], v[26:27]
	v_add_f32_e32 v0, v0, v29
	v_add_f32_e32 v0, v0, v30
	v_pk_mul_f32 v[46:47], v[14:15], v[14:15]
	v_add_f32_e32 v0, v0, v31
	v_add_f32_e32 v0, v0, v46
	v_pk_mul_f32 v[48:49], v[12:13], v[12:13]
	v_add_f32_e32 v0, v0, v47
	v_add_f32_e32 v0, v0, v48
	v_pk_mul_f32 v[50:51], v[18:19], v[18:19]
	v_add_f32_e32 v0, v0, v49
	v_add_f32_e32 v0, v0, v50
	v_pk_mul_f32 v[52:53], v[16:17], v[16:17]
	v_add_f32_e32 v0, v0, v51
	v_add_f32_e32 v0, v0, v52
	v_add_f32_e32 v0, v0, v53
	ds_bpermute_b32 v1, v54, v0
	v_mov_b32_e32 v20, 0x3727c5ac
	v_lshlrev_b64 v[30:31], 10, v[2:3]
	s_waitcnt lgkmcnt(0)
	v_add_f32_e32 v0, v0, v1
	ds_bpermute_b32 v1, v55, v0
	s_waitcnt lgkmcnt(0)
	v_add_f32_e32 v0, v0, v1
	ds_bpermute_b32 v1, v56, v0
	s_waitcnt lgkmcnt(0)
	v_add_f32_e32 v0, v0, v1
	ds_bpermute_b32 v1, v57, v0
	s_waitcnt lgkmcnt(0)
	v_add_f32_e32 v0, v0, v1
	ds_bpermute_b32 v1, v58, v0
	s_waitcnt lgkmcnt(0)
	v_add_f32_e32 v21, v0, v1
	ds_bpermute_b32 v28, v9, v21
	v_lshlrev_b64 v[0:1], 12, v[2:3]
	v_mov_b32_e32 v9, v11
	s_waitcnt lgkmcnt(0)
	v_add_f32_e32 v2, v21, v28
	v_fmac_f32_e32 v20, 0x3a800000, v2
	v_rsq_f32_e32 v28, v20
	v_lshl_add_u64 v[20:21], s[10:11], 0, v[0:1]
	v_pk_mul_f32 v[0:1], v[28:29], v[40:41] op_sel_hi:[0,1]
	v_pk_mul_f32 v[2:3], v[28:29], v[44:45] op_sel_hi:[0,1]
	v_pk_mul_f32 v[40:41], v[28:29], v[42:43] op_sel_hi:[0,1]
	v_pk_mul_f32 v[26:27], v[28:29], v[26:27] op_sel_hi:[0,1]
	s_waitcnt vmcnt(2)
	v_pk_fma_f32 v[4:5], v[4:5], v[0:1], v[22:23]
	s_waitcnt vmcnt(0)
	v_pk_fma_f32 v[0:1], v[32:33], v[2:3], v[36:37]
	v_pk_fma_f32 v[6:7], v[6:7], v[40:41], v[24:25]
	v_pk_fma_f32 v[2:3], v[34:35], v[26:27], v[38:39]
	v_lshlrev_b32_e32 v26, 2, v8
	s_cbranch_scc1 .LBB1_3
	v_mov_b32_e32 v27, v11
	v_lshl_add_u64 v[22:23], v[20:21], 0, v[26:27]
	global_store_dwordx4 v[22:23], v[4:7], off nt
	global_store_dwordx4 v[22:23], v[0:3], off offset:16 nt
.LBB1_3:
	s_load_dwordx2 s[10:11], s[0:1], 0x28
	s_cmp_lg_u64 s[4:5], 0
	s_cselect_b64 s[0:1], -1, 0
	s_cmp_eq_u64 s[4:5], 0
	v_lshl_add_u64 v[22:23], v[30:31], 1, s[4:5]
	v_lshlrev_b32_e32 v24, 1, v8
	s_cbranch_scc1 .LBB1_5
	v_mov_b32_e32 v25, 0
	v_cvt_pk_f16_f32 v32, v4, v5
	v_cvt_pk_f16_f32 v33, v6, v7
	v_cvt_pk_f16_f32 v34, v0, v1
	v_cvt_pk_f16_f32 v35, v2, v3
	v_lshl_add_u64 v[36:37], v[22:23], 0, v[24:25]
	global_store_dwordx4 v[36:37], v[32:35], off
.LBB1_5:
	s_waitcnt lgkmcnt(0)
	s_cmp_lg_u64 s[10:11], 0
	v_lshl_add_u64 v[30:31], s[10:11], 0, v[30:31]
	v_lshl_add_u64 v[32:33], s[6:7], 0, v[10:11]
	v_lshl_add_u64 v[10:11], s[8:9], 0, v[10:11]
	v_mov_b32_e32 v29, v28
	s_cselect_b64 s[4:5], -1, 0
	s_cmp_eq_u64 s[10:11], 0
	v_lshl_add_u64 v[8:9], v[30:31], 0, v[8:9]
	s_cbranch_scc1 .LBB1_7
	v_mov_b32_e32 v31, 0
	v_mov_b32_e32 v30, 0
	v_cvt_pk_fp8_f32 v30, v4, v5
	v_cvt_pk_fp8_f32 v31, v0, v1
	v_cvt_pk_fp8_f32 v30, v6, v7 op_sel:[0,0,1]
	v_cvt_pk_fp8_f32 v31, v2, v3 op_sel:[0,0,1]
	global_store_dwordx2 v[8:9], v[30:31], off
.LBB1_7:
	global_load_dwordx4 v[0:3], v[32:33], off offset:2064
	global_load_dwordx4 v[4:7], v[32:33], off offset:2048
	global_load_dwordx4 v[34:37], v[10:11], off offset:2048
	global_load_dwordx4 v[38:41], v[10:11], off offset:2064
	v_pk_mul_f32 v[10:11], v[28:29], v[14:15]
	v_pk_mul_f32 v[14:15], v[28:29], v[18:19]
	v_pk_mul_f32 v[12:13], v[28:29], v[12:13]
	v_pk_mul_f32 v[16:17], v[28:29], v[16:17]
	s_andn2_b64 vcc, exec, s[2:3]
	s_waitcnt vmcnt(1)
	v_pk_fma_f32 v[4:5], v[4:5], v[10:11], v[34:35]
	s_waitcnt vmcnt(0)
	v_pk_fma_f32 v[0:1], v[0:1], v[14:15], v[38:39]
	v_pk_fma_f32 v[6:7], v[6:7], v[12:13], v[36:37]
	v_pk_fma_f32 v[2:3], v[2:3], v[16:17], v[40:41]
	s_cbranch_vccnz .LBB1_9
	v_mov_b32_e32 v27, 0
	v_lshl_add_u64 v[10:11], v[20:21], 0, v[26:27]
	global_store_dwordx4 v[10:11], v[4:7], off offset:2048 nt
	global_store_dwordx4 v[10:11], v[0:3], off offset:2064 nt

	.amdhsa_kernel _Z4k_lnPKDF16_PKfS2_PfPDF16_Phi
		.amdhsa_group_segment_fixed_size 0
		.amdhsa_private_segment_fixed_size 0
		.amdhsa_kernarg_size 52
		.amdhsa_user_sgpr_count 2
		.amdhsa_user_sgpr_dispatch_ptr 0
		.amdhsa_user_sgpr_queue_ptr 0
		.amdhsa_user_sgpr_kernarg_segment_ptr 1
		.amdhsa_user_sgpr_dispatch_id 0
		.amdhsa_user_sgpr_kernarg_preload_length 0
		.amdhsa_user_sgpr_kernarg_preload_offset 0
		.amdhsa_user_sgpr_private_segment_size 0
		.amdhsa_uses_dynamic_stack 0
		.amdhsa_enable_private_segment 0
		.amdhsa_system_sgpr_workgroup_id_x 1
		.amdhsa_system_sgpr_workgroup_id_y 0
		.amdhsa_system_sgpr_workgroup_id_z 0
		.amdhsa_system_sgpr_workgroup_info 0
		.amdhsa_system_vgpr_workitem_id 0
		.amdhsa_next_free_vgpr 59
		.amdhsa_next_free_sgpr 12
		.amdhsa_accum_offset 60
		.amdhsa_reserve_vcc 1
		.amdhsa_float_round_mode_32 0
		.amdhsa_float_round_mode_16_64 0
		.amdhsa_float_denorm_mode_32 3
		.amdhsa_float_denorm_mode_16_64 3
		.amdhsa_dx10_clamp 1
		.amdhsa_ieee_mode 1
		.amdhsa_fp16_overflow 0
		.amdhsa_tg_split 0
		.amdhsa_exception_fp_ieee_invalid_op 0
		.amdhsa_exception_fp_denorm_src 0
		.amdhsa_exception_fp_ieee_div_zero 0
		.amdhsa_exception_fp_ieee_overflow 0
		.amdhsa_exception_fp_ieee_underflow 0
		.amdhsa_exception_fp_ieee_inexact 0
		.amdhsa_exception_int_div_zero 0
	.end_amdhsa_kernel

.LBB3_4:
	s_lshl_b32 s18, s24, 8
	s_and_b32 s18, s18, 0x300
	s_lshl_b64 s[0:1], s[0:1], 10
	s_or_b32 s0, s0, s18
	s_lshl_b32 s18, s33, 5
	s_add_u32 s18, s0, s18
	v_and_b32_e32 v203, 31, v0
	s_addc_u32 s19, s1, 0
	v_or_b32_e32 v2, s18, v203
	v_mov_b32_e32 v3, s19
	v_lshrrev_b32_e32 v204, 5, v1
	v_lshlrev_b64 v[4:5], 10, v[2:3]
	v_lshlrev_b64 v[2:3], 12, v[2:3]
	v_lshl_add_u64 v[2:3], s[14:15], 0, v[2:3]
	v_lshlrev_b32_e32 v28, 4, v204
	v_mov_b32_e32 v29, 0
	v_lshl_add_u64 v[26:27], v[2:3], 0, v[28:29]
	v_lshl_add_u64 v[2:3], s[8:9], 0, v[4:5]
	v_lshl_add_u64 v[2:3], v[2:3], 0, s[6:7]
	v_and_b32_e32 v28, 32, v0
	v_lshl_add_u64 v[40:41], v[2:3], 0, v[28:29]
	global_load_dwordx4 v[100:103], v[40:41], off offset:16
	global_load_dwordx4 v[96:99], v[40:41], off
	global_load_dwordx4 v[64:67], v[26:27], off
	global_load_dwordx4 v[68:71], v[26:27], off offset:32
	global_load_dwordx4 v[2:5], v[26:27], off offset:128
	global_load_dwordx4 v[6:9], v[26:27], off offset:160
	global_load_dwordx4 v[72:75], v[26:27], off offset:64
	global_load_dwordx4 v[76:79], v[26:27], off offset:96
	global_load_dwordx4 v[10:13], v[26:27], off offset:192
	global_load_dwordx4 v[14:17], v[26:27], off offset:224
	v_mul_hi_u32_u24_e32 v21, 0x1800, v20
	s_and_b64 vcc, exec, s[4:5]
	v_mul_u32_u24_e32 v20, 0x1800, v20
	s_cbranch_vccnz .LBB3_6
	s_mov_b64 s[0:1], 0x20000
	s_cmp_lg_u32 0, -1
	v_lshl_add_u64 v[26:27], v[22:23], 0, s[0:1]
	s_cselect_b32 s0, 0, 0
	s_add_i32 s0, s0, s35
	s_addk_i32 s0, 0x4000
	s_mov_b32 m0, s0
	s_nop 0
	global_load_lds_dwordx4 v[26:27], off
.LBB3_6:
	v_lshlrev_b32_e32 v104, 3, v24
	v_or_b32_e32 v24, s18, v30
	v_mov_b32_e32 v25, s19
	v_lshlrev_b64 v[24:25], 12, v[24:25]
	v_lshl_add_u64 v[80:81], s[14:15], 0, v[24:25]
	v_lshrrev_b32_e32 v106, 2, v203
	v_lshlrev_b32_e32 v24, 1, v204
	v_bfe_u32 v25, v203, 2, 2
	s_lshl_b32 s7, s33, 13
	v_bitop3_b32 v26, v24, v106, 3 bitop3:0x78
	v_bitop3_b32 v24, v24, v25, 1 bitop3:0x36
	s_cmp_lg_u32 0, -1
	v_lshlrev_b32_e32 v218, 4, v24
	v_bitop3_b32 v24, v30, v0, 15 bitop3:0x78
	s_cselect_b32 s0, 0, 0
	v_lshlrev_b32_e32 v28, 4, v24
	s_add_i32 s23, s0, s7
	v_lshl_add_u64 v[164:165], v[80:81], 0, v[28:29]
	s_mov_b64 s[0:1], 0x100
	v_and_b32_e32 v105, 15, v0
	v_lshl_add_u64 v[24:25], v[164:165], 0, s[0:1]
	s_add_i32 s36, s23, 0x14800
	s_mov_b32 m0, s36
	s_nop 0
	global_load_lds_dwordx4 v[24:25], off nt
	v_bitop3_b32 v24, v30, v105, 4 bitop3:0x36
	v_lshlrev_b32_e32 v28, 4, v24
	v_lshl_add_u64 v[24:25], v[80:81], 0, v[28:29]
	s_mov_b64 s[8:9], 0x4100
	v_lshlrev_b32_e32 v217, 4, v26
	v_lshl_add_u64 v[26:27], v[24:25], 0, s[8:9]
	s_add_i32 s8, s23, 0x14c00
	s_mov_b32 m0, s8
	s_nop 0
	global_load_lds_dwordx4 v[26:27], off nt
	v_bitop3_b32 v26, v30, v105, 8 bitop3:0x36
	v_lshlrev_b32_e32 v28, 4, v26
	v_lshl_add_u64 v[26:27], v[80:81], 0, v[28:29]
	s_mov_b64 s[14:15], 0x8100
	v_bitop3_b32 v28, v30, v105, 12 bitop3:0x36
	v_lshl_add_u64 v[82:83], v[26:27], 0, s[14:15]
	s_add_i32 s14, s23, 0x15000
	s_mov_b32 m0, s14
	s_nop 0
	global_load_lds_dwordx4 v[82:83], off nt
	v_lshlrev_b32_e32 v28, 4, v28
	v_lshl_add_u64 v[28:29], v[80:81], 0, v[28:29]
	s_mov_b64 s[14:15], 0xc100
	v_lshl_add_u64 v[80:81], v[28:29], 0, s[14:15]
	s_add_i32 s14, s23, 0x15400
	s_mov_b32 m0, s14
	s_nop 0
	global_load_lds_dwordx4 v[80:81], off nt
	s_mov_b64 s[26:27], 0x10100
	v_lshl_add_u64 v[80:81], v[164:165], 0, s[26:27]
	s_add_i32 s26, s23, 0x15800
	s_mov_b32 m0, s26
	s_nop 0
	global_load_lds_dwordx4 v[80:81], off nt
	s_mov_b64 s[28:29], 0x14100
	v_lshl_add_u64 v[80:81], v[24:25], 0, s[28:29]
	s_add_i32 s28, s23, 0x15c00
	s_mov_b32 m0, s28
	s_nop 0
	global_load_lds_dwordx4 v[80:81], off nt
	s_mov_b64 s[30:31], 0x18100
	v_lshl_add_u64 v[80:81], v[26:27], 0, s[30:31]
	s_add_i32 s30, s23, 0x16000
	s_mov_b32 m0, s30
	s_nop 0
	global_load_lds_dwordx4 v[80:81], off nt
	s_mov_b64 s[30:31], 0x1c100
	v_lshl_add_u32 v216, v203, 6, 0
	v_lshl_add_u64 v[80:81], v[28:29], 0, s[30:31]
	s_add_i32 s23, s23, 0x16400
	s_mov_b32 m0, s23
	s_nop 0
	global_load_lds_dwordx4 v[80:81], off nt
	s_waitcnt vmcnt(9) lgkmcnt(0)
	s_barrier
	v_add_u32_e32 v209, v216, v217
	v_add_u32_e32 v210, v216, v218
	ds_read_b128 v[80:83], v209
	ds_read_b128 v[88:91], v209 offset:2048
	ds_read_b128 v[84:87], v210
	ds_read_b128 v[92:95], v210 offset:2048
	v_mov_b32_e32 v219, 0x7f7f7f7f
	v_mov_b32_e32 v220, 0x7c7c7c7c
	s_waitcnt vmcnt(10) lgkmcnt(1)
	v_mfma_scale_f32_32x32x64_f8f6f4 v[64:79], v[80:87], v[96:103], v[64:79], v219, v220 op_sel_hi:[0,0,0]
	s_waitcnt vmcnt(8) lgkmcnt(0)
	v_mfma_scale_f32_32x32x64_f8f6f4 v[2:17], v[88:95], v[96:103], v[2:17], v219, v220 op_sel_hi:[0,0,0]
	s_mov_b32 s39, 0x3fb8aa3b
	s_nop 15
	s_nop 15
	s_nop 15
	s_nop 15
	s_nop 15
	s_nop 15
	s_waitcnt vmcnt(0) lgkmcnt(0)
	s_barrier
	v_lshlrev_b32_e32 v31, 2, v204
	v_max_f32_e32 v80, v65, v65
	v_max_f32_e32 v81, v64, v64
	v_max_f32_e32 v80, v81, v80
	v_max3_f32 v81, v66, v67, v3
	v_max3_f32 v80, v80, v2, v4
	v_max3_f32 v80, v80, v5, v68
	v_max3_f32 v81, v81, v70, v71
	v_max3_f32 v80, v80, v69, v6
	v_max3_f32 v81, v81, v8, v9
	v_max3_f32 v80, v80, v7, v72
	v_max3_f32 v81, v81, v74, v75
	v_max3_f32 v80, v80, v73, v10
	v_max3_f32 v81, v81, v12, v13
	v_max3_f32 v80, v80, v11, v76
	v_max3_f32 v81, v81, v78, v79
	v_max3_f32 v80, v80, v77, v14
	v_max3_f32 v81, v81, v16, v17
	v_max3_f32 v80, v80, v15, v81
	v_mov_b32_e32 v81, v80
	s_nop 1
	v_permlane32_swap_b32_e32 v80, v81
	v_max_f32_e32 v81, v81, v81
	v_max_f32_e32 v80, v80, v80
	v_max_f32_e32 v80, v80, v81
	v_mul_f32_e32 v208, 0x3fb8aa3b, v80
	s_mov_b32 s48, 0
	s_mov_b32 s38, -1
	s_mov_b64 s[0:1], 0x4000
	s_mov_b64 s[8:9], 0x8000
	s_mov_b64 s[24:25], 0xc000
	s_mov_b64 s[14:15], 0x10000
	s_mov_b64 s[26:27], 0x14000
	s_mov_b64 s[28:29], 0x18000
	s_mov_b64 s[30:31], 0x1c000
	v_fma_f32 v64, v64, s39, -v208
	v_fma_f32 v2, v2, s39, -v208
	v_fma_f32 v65, v65, s39, -v208
	v_fma_f32 v3, v3, s39, -v208
	v_fma_f32 v66, v66, s39, -v208
	v_fma_f32 v4, v4, s39, -v208
	v_fma_f32 v67, v67, s39, -v208
	v_fma_f32 v5, v5, s39, -v208
	v_fma_f32 v68, v68, s39, -v208
	v_fma_f32 v6, v6, s39, -v208
	v_fma_f32 v69, v69, s39, -v208
	v_fma_f32 v7, v7, s39, -v208
	v_fma_f32 v70, v70, s39, -v208
	v_fma_f32 v8, v8, s39, -v208
	v_fma_f32 v71, v71, s39, -v208
	v_fma_f32 v9, v9, s39, -v208
	v_fma_f32 v72, v72, s39, -v208
	v_fma_f32 v10, v10, s39, -v208
	v_fma_f32 v73, v73, s39, -v208
	v_fma_f32 v11, v11, s39, -v208
	v_fma_f32 v74, v74, s39, -v208
	v_fma_f32 v12, v12, s39, -v208
	v_fma_f32 v75, v75, s39, -v208
	v_fma_f32 v13, v13, s39, -v208
	v_fma_f32 v76, v76, s39, -v208
	v_fma_f32 v14, v14, s39, -v208
	v_fma_f32 v77, v77, s39, -v208
	v_fma_f32 v78, v78, s39, -v208
	v_fma_f32 v79, v79, s39, -v208
	v_fma_f32 v94, v15, s39, -v208
	v_fma_f32 v16, v16, s39, -v208
	v_fma_f32 v15, v17, s39, -v208
	s_and_b64 vcc, exec, s[4:5]
	s_cbranch_vccnz .LBB3_8
	s_mov_b64 s[42:43], 0x30000
	v_lshl_add_u64 v[22:23], v[22:23], 0, s[42:43]
	s_mov_b32 m0, s37
	s_nop 0
	global_load_lds_dwordx4 v[22:23], off
.LBB3_8:
	v_lshl_add_u64 v[178:179], v[24:25], 0, s[0:1]
	s_and_b32 s0, s40, 0x3fffffc0
	s_lshl_b32 s0, s0, 2
	s_add_i32 s23, s0, 0
	s_add_i32 s0, s7, 0
	s_add_i32 s0, s0, 0x14800
	v_lshlrev_b32_e32 v0, 8, v0
	s_cmp_lg_u32 0, -1
	v_lshl_add_u64 v[174:175], v[28:29], 0, s[24:25]
	v_exp_f32_e32 v80, v64
	v_exp_f32_e32 v64, v2
	v_lshlrev_b32_e32 v2, 10, v106
	v_and_b32_e32 v0, 0x300, v0
	s_cselect_b32 s24, 0, 0
	v_add3_u32 v222, s0, v2, v0
	s_add_i32 s0, s24, s35
	s_add_i32 s24, s24, s7
	v_lshl_add_u64 v[166:167], v[28:29], 0, s[30:31]
	s_add_i32 s0, s0, 0x8000
	s_add_i32 s30, s24, 0x14c00
	s_add_i32 s31, s24, 0x15000
	s_add_i32 s40, s24, 0x15400
	s_add_i32 s41, s24, 0x15800
	s_add_i32 s42, s24, 0x15c00
	s_add_i32 s43, s24, 0x16000
	s_add_i32 s44, s24, 0x16400
	v_lshlrev_b32_e32 v0, 5, v30
	v_lshrrev_b32_e32 v2, 2, v105
	s_add_u32 s20, s6, s20
	v_and_b32_e32 v0, 32, v0
	v_or_b32_e32 v2, v31, v2
	s_addc_u32 s21, 0, s21
	s_lshl_b32 s2, s2, 4
	v_lshl_add_u64 v[176:177], v[26:27], 0, s[8:9]
	v_add_u32_e32 v0, 0, v0
	v_lshlrev_b32_e32 v2, 6, v2
	s_mov_b64 s[8:9], 0x60000
	s_and_b32 s2, s2, 0x780
	v_exp_f32_e32 v81, v65
	v_exp_f32_e32 v65, v3
	v_add3_u32 v207, v0, v104, v2
	v_lshl_add_u64 v[2:3], v[162:163], 0, s[8:9]
	s_mov_b32 m0, s0
	s_nop 0
	global_load_lds_dwordx4 v[2:3], off
	v_add_lshl_u32 v184, v202, s3, 10
	v_mov_b32_e32 v185, 0
	s_add_u32 s2, s22, s2
	v_exp_f32_e32 v82, v66
	v_exp_f32_e32 v66, v4
	v_xor_b32_e32 v4, v204, v105
	ds_read_b128 v[112:115], v209 offset:8192
	ds_read_b128 v[104:107], v209 offset:10240
	ds_read_b128 v[116:119], v210 offset:8192
	ds_read_b128 v[108:111], v210 offset:10240
	v_cmp_gt_u32_e64 s[0:1], 32, v1
	v_lshl_add_u64 v[0:1], s[20:21], 0, v[184:185]
	s_addc_u32 s3, 0, 0
	v_lshl_add_u64 v[0:1], v[0:1], 0, v[18:19]
	s_add_u32 s2, s2, s46
	v_lshl_add_u64 v[0:1], s[10:11], 0, v[0:1]
	s_addc_u32 s3, s3, s45
	v_exp_f32_e32 v83, v67
	v_exp_f32_e32 v67, v5
	v_exp_f32_e32 v84, v68
	v_exp_f32_e32 v68, v6
	v_exp_f32_e32 v85, v69
	v_exp_f32_e32 v69, v7
	v_exp_f32_e32 v86, v70
	v_exp_f32_e32 v70, v8
	v_exp_f32_e32 v87, v71
	v_exp_f32_e32 v71, v9
	v_exp_f32_e32 v88, v72
	v_exp_f32_e32 v72, v10
	v_exp_f32_e32 v89, v73
	v_exp_f32_e32 v73, v11
	v_exp_f32_e32 v90, v74
	v_exp_f32_e32 v74, v12
	v_exp_f32_e32 v91, v75
	v_exp_f32_e32 v75, v13
	v_exp_f32_e32 v92, v76
	v_exp_f32_e32 v76, v14
	v_exp_f32_e32 v93, v77
	v_exp_f32_e32 v77, v94
	v_exp_f32_e32 v94, v78
	v_exp_f32_e32 v78, v16
	v_exp_f32_e32 v95, v79
	v_exp_f32_e32 v79, v15
	v_lshl_add_u64 v[180:181], v[0:1], 0, s[14:15]
	v_lshl_add_u64 v[0:1], s[2:3], 0, v[20:21]
	v_mov_b32_e32 v161, v185
	s_waitcnt vmcnt(2) lgkmcnt(0)
	s_barrier
	v_lshlrev_b32_e32 v223, 4, v4
	v_lshl_add_u64 v[0:1], v[0:1], 0, v[160:161]
	v_xor_b32_e32 v2, 0x80, v223
	v_xor_b32_e32 v3, 32, v223
	v_xor_b32_e32 v4, 0xa0, v223
	v_xor_b32_e32 v5, 64, v223
	v_xor_b32_e32 v6, 0xc0, v223
	v_xor_b32_e32 v7, 0x60, v223
	v_xor_b32_e32 v8, 0xe0, v223
	v_lshl_add_u64 v[0:1], s[12:13], 0, v[0:1]
	v_lshl_add_u64 v[172:173], v[164:165], 0, s[14:15]
	v_lshl_add_u64 v[170:171], v[24:25], 0, s[26:27]
	v_lshl_add_u64 v[168:169], v[26:27], 0, s[28:29]
	v_lshl_add_u32 v206, v203, 2, s23
	v_lshl_add_u32 v205, v31, 2, s23
	v_lshl_add_u64 v[182:183], v[0:1], 0, s[8:9]
	s_movk_i32 s45, 0x4000
	s_movk_i32 s47, 0x2000
	s_mov_b64 s[2:3], 0
	s_mov_b32 s46, 0x41000000
	s_mov_b64 s[10:11], 0x30000
	s_mov_b64 s[12:13], 0x300
	s_mov_b64 s[14:15], 0x40000
	s_mov_b64 s[20:21], 0xc0000
	s_mov_b64 s[22:23], 0x400
	s_mov_b64 s[24:25], 0x20000
	v_add_u32_e32 v161, v222, v2
	v_add_u32_e32 v184, v222, v3
	v_add_u32_e32 v211, v222, v4
	v_add_u32_e32 v212, v222, v5
	v_add_u32_e32 v213, v222, v6
	v_add_u32_e32 v214, v222, v7
	v_add_u32_e32 v215, v222, v8
	v_mov_b32_e32 v0, v185
	v_mov_b32_e32 v1, v185
	v_mov_b32_e32 v2, v185
	v_mov_b32_e32 v3, v185
	v_mov_b32_e32 v4, v185
	v_mov_b32_e32 v5, v185
	v_mov_b32_e32 v6, v185
	v_mov_b32_e32 v7, v185
	v_mov_b32_e32 v8, v185
	v_mov_b32_e32 v9, v185
	v_mov_b32_e32 v10, v185
	v_mov_b32_e32 v11, v185
	v_mov_b32_e32 v12, v185
	v_mov_b32_e32 v13, v185
	v_mov_b32_e32 v14, v185
	v_mov_b32_e32 v15, v185
	v_mov_b32_e32 v16, v185
	v_mov_b32_e32 v17, v185
	v_mov_b32_e32 v18, v185
	v_mov_b32_e32 v19, v185
	v_mov_b32_e32 v20, v185
	v_mov_b32_e32 v21, v185
	v_mov_b32_e32 v22, v185
	v_mov_b32_e32 v23, v185
	v_mov_b32_e32 v24, v185
	v_mov_b32_e32 v25, v185
	v_mov_b32_e32 v26, v185
	v_mov_b32_e32 v27, v185
	v_mov_b32_e32 v28, v185
	v_mov_b32_e32 v29, v185
	v_mov_b32_e32 v30, v185
	v_mov_b32_e32 v31, v185
	v_add_u32_e32 v221, v222, v223
	ds_read_b128 v[48:51], v221
	ds_read_b128 v[32:35], v161
	ds_read_b128 v[52:55], v184
	ds_read_b128 v[36:39], v211
	ds_read_b128 v[56:59], v212
	ds_read_b128 v[40:43], v213
	ds_read_b128 v[60:63], v214
	ds_read_b128 v[44:47], v215
	s_waitcnt lgkmcnt(0)
	s_mov_b64 s[52:53], 0x200
	v_lshl_add_u64 v[224:225], v[164:165], 0, s[52:53]
	s_mov_b32 m0, s36
	s_nop 0
	global_load_lds_dwordx4 v[224:225], off nt
	v_lshl_add_u64 v[224:225], v[178:179], 0, s[52:53]
	s_mov_b32 m0, s30
	s_nop 0
	global_load_lds_dwordx4 v[224:225], off nt
	v_lshl_add_u64 v[224:225], v[176:177], 0, s[52:53]
	s_mov_b32 m0, s31
	s_nop 0
	global_load_lds_dwordx4 v[224:225], off nt
	v_lshl_add_u64 v[224:225], v[174:175], 0, s[52:53]
	s_mov_b32 m0, s40
	s_nop 0
	global_load_lds_dwordx4 v[224:225], off nt
	v_lshl_add_u64 v[224:225], v[172:173], 0, s[52:53]
	s_mov_b32 m0, s41
	s_nop 0
	global_load_lds_dwordx4 v[224:225], off nt
	v_lshl_add_u64 v[224:225], v[170:171], 0, s[52:53]
	s_mov_b32 m0, s42
	s_nop 0
	global_load_lds_dwordx4 v[224:225], off nt
	v_lshl_add_u64 v[224:225], v[168:169], 0, s[52:53]
	s_mov_b32 m0, s43
	s_nop 0
	global_load_lds_dwordx4 v[224:225], off nt
	v_lshl_add_u64 v[224:225], v[166:167], 0, s[52:53]
	s_mov_b32 m0, s44
	s_nop 0
	global_load_lds_dwordx4 v[224:225], off nt

	.amdhsa_kernel _Z6k_attnILi1024ELi1024ELi1024ELi1024ELi3072ELi1024ELb1ELb1EEvPKDF16_S1_S1_PKfPDF16_
		.amdhsa_group_segment_fixed_size 0
		.amdhsa_private_segment_fixed_size 0
		.amdhsa_kernarg_size 40
		.amdhsa_user_sgpr_count 2
		.amdhsa_user_sgpr_dispatch_ptr 0
		.amdhsa_user_sgpr_queue_ptr 0
		.amdhsa_user_sgpr_kernarg_segment_ptr 1
		.amdhsa_user_sgpr_dispatch_id 0
		.amdhsa_user_sgpr_kernarg_preload_length 0
		.amdhsa_user_sgpr_kernarg_preload_offset 0
		.amdhsa_user_sgpr_private_segment_size 0
		.amdhsa_uses_dynamic_stack 0
		.amdhsa_enable_private_segment 0
		.amdhsa_system_sgpr_workgroup_id_x 1
		.amdhsa_system_sgpr_workgroup_id_y 0
		.amdhsa_system_sgpr_workgroup_id_z 0
		.amdhsa_system_sgpr_workgroup_info 0
		.amdhsa_system_vgpr_workitem_id 0
		.amdhsa_next_free_vgpr 226
		.amdhsa_next_free_sgpr 54
		.amdhsa_accum_offset 228
		.amdhsa_reserve_vcc 1
		.amdhsa_float_round_mode_32 0
		.amdhsa_float_round_mode_16_64 0
		.amdhsa_float_denorm_mode_32 3
		.amdhsa_float_denorm_mode_16_64 3
		.amdhsa_dx10_clamp 1
		.amdhsa_ieee_mode 1
		.amdhsa_fp16_overflow 0
		.amdhsa_tg_split 0
		.amdhsa_exception_fp_ieee_invalid_op 0
		.amdhsa_exception_fp_denorm_src 0
		.amdhsa_exception_fp_ieee_div_zero 0
		.amdhsa_exception_fp_ieee_overflow 0
		.amdhsa_exception_fp_ieee_underflow 0
		.amdhsa_exception_fp_ieee_inexact 0
		.amdhsa_exception_int_div_zero 0
	.end_amdhsa_kernel

.LBB4_8:
	s_lshl_b32 s10, s18, 7
	v_lshlrev_b32_e32 v0, 3, v1
	s_add_i32 s10, s10, s1
	v_lshl_or_b32 v0, s16, 7, v0
	v_or_b32_e32 v42, s10, v42
	v_or_b32_e32 v38, s0, v0
	v_mov_b32_e32 v39, 0
	s_waitcnt lgkmcnt(0)
	v_mad_i64_i32 v[40:41], s[0:1], v42, s2, v[38:39]
	v_mov_b32_e32 v33, v35
	v_lshl_add_u64 v[0:1], v[40:41], 1, s[8:9]
	s_barrier
	s_nop 15
	s_nop 15
	s_nop 15
	global_load_dwordx4 v[34:37], v[0:1], off
	s_cmp_lg_u64 s[6:7], 0
	s_mov_b32 s10, s3
	s_mov_b32 s11, s3
	s_cselect_b64 s[12:13], -1, 0
	s_cmp_eq_u64 s[6:7], 0
	v_lshl_add_u64 v[0:1], v[38:39], 2, s[6:7]
	v_pk_mul_f32 v[32:33], s[2:3], v[32:33] op_sel:[1,0]
	v_pk_mul_f32 v[30:31], s[2:3], v[30:31] op_sel:[1,0]
	v_pk_mul_f32 v[28:29], s[2:3], v[28:29] op_sel:[1,0]
	v_pk_mul_f32 v[26:27], s[2:3], v[26:27] op_sel:[1,0]
	s_cbranch_scc1 .LBB4_10
	global_load_dwordx4 v[44:47], v[0:1], off
	global_load_dwordx4 v[48:51], v[0:1], off offset:16
	s_waitcnt vmcnt(0)
	v_pk_add_f32 v[32:33], v[32:33], v[46:47]
	v_pk_add_f32 v[30:31], v[30:31], v[44:45]
	v_pk_add_f32 v[28:29], v[28:29], v[50:51]
	v_pk_add_f32 v[26:27], v[26:27], v[48:49]

	.amdhsa_kernel _ZN2g811k_gemm128f8INS_6EpiResEEEvPKhS3_iiiT_
		.amdhsa_group_segment_fixed_size 0
		.amdhsa_private_segment_fixed_size 0
		.amdhsa_kernarg_size 64
		.amdhsa_user_sgpr_count 2
		.amdhsa_user_sgpr_dispatch_ptr 0
		.amdhsa_user_sgpr_queue_ptr 0
		.amdhsa_user_sgpr_kernarg_segment_ptr 1
		.amdhsa_user_sgpr_dispatch_id 0
		.amdhsa_user_sgpr_kernarg_preload_length 0
		.amdhsa_user_sgpr_kernarg_preload_offset 0
		.amdhsa_user_sgpr_private_segment_size 0
		.amdhsa_uses_dynamic_stack 0
		.amdhsa_enable_private_segment 0
		.amdhsa_system_sgpr_workgroup_id_x 1
		.amdhsa_system_sgpr_workgroup_id_y 0
		.amdhsa_system_sgpr_workgroup_id_z 0
		.amdhsa_system_sgpr_workgroup_info 0
		.amdhsa_system_vgpr_workitem_id 0
		.amdhsa_next_free_vgpr 98
		.amdhsa_next_free_sgpr 28
		.amdhsa_accum_offset 100
		.amdhsa_reserve_vcc 1
		.amdhsa_float_round_mode_32 0
		.amdhsa_float_round_mode_16_64 0
		.amdhsa_float_denorm_mode_32 3
		.amdhsa_float_denorm_mode_16_64 3
		.amdhsa_dx10_clamp 1
		.amdhsa_ieee_mode 1
		.amdhsa_fp16_overflow 0
		.amdhsa_tg_split 0
		.amdhsa_exception_fp_ieee_invalid_op 0
		.amdhsa_exception_fp_denorm_src 0
		.amdhsa_exception_fp_ieee_div_zero 0
		.amdhsa_exception_fp_ieee_overflow 0
		.amdhsa_exception_fp_ieee_underflow 0
		.amdhsa_exception_fp_ieee_inexact 0
		.amdhsa_exception_int_div_zero 0
	.end_amdhsa_kernel

.LBB6_4:
	s_lshl_b32 s18, s20, 8
	s_and_b32 s18, s18, 0x300
	s_lshl_b64 s[0:1], s[0:1], 10
	s_or_b32 s0, s0, s18
	s_lshl_b32 s18, s33, 5
	s_add_u32 s18, s0, s18
	v_and_b32_e32 v203, 31, v0
	s_addc_u32 s19, s1, 0
	v_or_b32_e32 v2, s18, v203
	v_mov_b32_e32 v3, s19
	v_lshrrev_b32_e32 v204, 5, v1
	v_lshlrev_b64 v[4:5], 13, v[2:3]
	v_lshlrev_b64 v[2:3], 10, v[2:3]
	v_lshl_add_u64 v[4:5], s[14:15], 0, v[4:5]
	v_lshlrev_b32_e32 v26, 4, v204
	v_mov_b32_e32 v27, 0
	v_lshl_add_u64 v[2:3], s[8:9], 0, v[2:3]
	v_lshl_add_u64 v[24:25], v[4:5], 0, v[26:27]
	v_lshl_add_u64 v[2:3], v[2:3], 0, s[6:7]
	v_and_b32_e32 v26, 32, v0
	v_lshl_add_u64 v[30:31], v[2:3], 0, v[26:27]
	global_load_dwordx4 v[100:103], v[30:31], off offset:16
	global_load_dwordx4 v[96:99], v[30:31], off
	global_load_dwordx4 v[64:67], v[24:25], off
	global_load_dwordx4 v[68:71], v[24:25], off offset:32
	global_load_dwordx4 v[2:5], v[24:25], off offset:128
	global_load_dwordx4 v[6:9], v[24:25], off offset:160
	global_load_dwordx4 v[72:75], v[24:25], off offset:64
	global_load_dwordx4 v[76:79], v[24:25], off offset:96
	global_load_dwordx4 v[10:13], v[24:25], off offset:192
	global_load_dwordx4 v[14:17], v[24:25], off offset:224
	s_and_b64 vcc, exec, s[4:5]
	s_cbranch_vccnz .LBB6_6
	s_mov_b64 s[0:1], 0x20000
	s_cmp_lg_u32 0, -1
	v_lshl_add_u64 v[24:25], v[20:21], 0, s[0:1]
	s_cselect_b32 s0, 0, 0
	s_add_i32 s0, s0, s36
	s_addk_i32 s0, 0x4000
	s_mov_b32 m0, s0
	s_nop 0
	global_load_lds_dwordx4 v[24:25], off
.LBB6_6:
	v_lshlrev_b32_e32 v30, 3, v22
	v_or_b32_e32 v22, s18, v28
	v_mov_b32_e32 v23, s19
	v_lshlrev_b64 v[22:23], 13, v[22:23]
	v_lshl_add_u64 v[80:81], s[14:15], 0, v[22:23]
	v_lshrrev_b32_e32 v104, 2, v203
	v_lshlrev_b32_e32 v22, 1, v204
	v_bfe_u32 v23, v203, 2, 2
	s_lshl_b32 s7, s33, 13
	v_bitop3_b32 v24, v22, v104, 3 bitop3:0x78
	v_bitop3_b32 v22, v22, v23, 1 bitop3:0x36
	s_cmp_lg_u32 0, -1
	v_lshlrev_b32_e32 v218, 4, v22
	v_bitop3_b32 v22, v28, v0, 15 bitop3:0x78
	s_cselect_b32 s0, 0, 0
	v_lshlrev_b32_e32 v26, 4, v22
	s_add_i32 s41, s0, s7
	v_lshl_add_u64 v[164:165], v[80:81], 0, v[26:27]
	s_mov_b64 s[0:1], 0x100
	v_and_b32_e32 v31, 15, v0
	v_lshl_add_u64 v[22:23], v[164:165], 0, s[0:1]
	s_add_i32 s38, s41, 0x14800
	s_mov_b32 m0, s38
	s_nop 0
	global_load_lds_dwordx4 v[22:23], off nt
	v_bitop3_b32 v22, v28, v31, 4 bitop3:0x36
	v_lshlrev_b32_e32 v26, 4, v22
	v_lshl_add_u64 v[22:23], v[80:81], 0, v[26:27]
	s_mov_b64 s[8:9], 0x8100
	v_lshlrev_b32_e32 v217, 4, v24
	v_lshl_add_u64 v[24:25], v[22:23], 0, s[8:9]
	s_add_i32 s8, s41, 0x14c00
	s_mov_b32 m0, s8
	s_nop 0
	global_load_lds_dwordx4 v[24:25], off nt
	v_bitop3_b32 v24, v28, v31, 8 bitop3:0x36
	v_lshlrev_b32_e32 v26, 4, v24
	v_lshl_add_u64 v[24:25], v[80:81], 0, v[26:27]
	s_mov_b64 s[8:9], 0x10100
	v_bitop3_b32 v26, v28, v31, 12 bitop3:0x36
	v_lshl_add_u64 v[82:83], v[24:25], 0, s[8:9]
	s_add_i32 s8, s41, 0x15000
	s_mov_b32 m0, s8
	s_nop 0
	global_load_lds_dwordx4 v[82:83], off nt
	v_lshlrev_b32_e32 v26, 4, v26
	v_lshl_add_u64 v[26:27], v[80:81], 0, v[26:27]
	s_mov_b64 s[8:9], 0x18100
	v_lshl_add_u64 v[80:81], v[26:27], 0, s[8:9]
	s_add_i32 s8, s41, 0x15400
	s_mov_b32 m0, s8
	s_nop 0
	global_load_lds_dwordx4 v[80:81], off nt
	s_mov_b64 s[14:15], 0x20100
	v_lshl_add_u64 v[80:81], v[164:165], 0, s[14:15]
	s_add_i32 s14, s41, 0x15800
	s_mov_b32 m0, s14
	s_nop 0
	global_load_lds_dwordx4 v[80:81], off nt
	s_mov_b64 s[14:15], 0x28100
	v_lshl_add_u64 v[80:81], v[22:23], 0, s[14:15]
	s_add_i32 s14, s41, 0x15c00
	s_mov_b32 m0, s14
	s_nop 0
	global_load_lds_dwordx4 v[80:81], off nt
	s_mov_b64 s[34:35], 0x30100
	v_lshl_add_u64 v[80:81], v[24:25], 0, s[34:35]
	s_add_i32 s34, s41, 0x16000
	s_mov_b32 m0, s34
	s_nop 0
	global_load_lds_dwordx4 v[80:81], off nt
	s_mov_b64 s[34:35], 0x38100
	v_lshl_add_u32 v216, v203, 6, 0
	v_lshl_add_u64 v[80:81], v[26:27], 0, s[34:35]
	s_add_i32 s41, s41, 0x16400
	s_mov_b32 m0, s41
	s_nop 0
	global_load_lds_dwordx4 v[80:81], off nt
	s_waitcnt vmcnt(9) lgkmcnt(0)
	s_barrier
	v_add_u32_e32 v209, v216, v217
	v_add_u32_e32 v210, v216, v218
	ds_read_b128 v[80:83], v209
	ds_read_b128 v[88:91], v209 offset:2048
	ds_read_b128 v[84:87], v210
	ds_read_b128 v[92:95], v210 offset:2048
	v_mov_b32_e32 v219, 0x7f7f7f7f
	v_mov_b32_e32 v220, 0x7c7c7c7c
	s_waitcnt vmcnt(10) lgkmcnt(1)
	v_mfma_scale_f32_32x32x64_f8f6f4 v[64:79], v[80:87], v[96:103], v[64:79], v219, v220 op_sel_hi:[0,0,0]
	s_waitcnt vmcnt(8) lgkmcnt(0)
	v_mfma_scale_f32_32x32x64_f8f6f4 v[2:17], v[88:95], v[96:103], v[2:17], v219, v220 op_sel_hi:[0,0,0]
	s_mov_b32 s41, 0x3fb8aa3b
	s_nop 15
	s_nop 15
	s_nop 15
	s_nop 15
	s_nop 15
	s_nop 15
	s_waitcnt vmcnt(0) lgkmcnt(0)
	s_barrier
	v_lshlrev_b32_e32 v29, 2, v204
	v_max_f32_e32 v80, v65, v65
	v_max_f32_e32 v81, v64, v64
	v_max_f32_e32 v80, v81, v80
	v_max3_f32 v81, v66, v67, v3
	v_max3_f32 v80, v80, v2, v4
	v_max3_f32 v80, v80, v5, v68
	v_max3_f32 v81, v81, v70, v71
	v_max3_f32 v80, v80, v69, v6
	v_max3_f32 v81, v81, v8, v9
	v_max3_f32 v80, v80, v7, v72
	v_max3_f32 v81, v81, v74, v75
	v_max3_f32 v80, v80, v73, v10
	v_max3_f32 v81, v81, v12, v13
	v_max3_f32 v80, v80, v11, v76
	v_max3_f32 v81, v81, v78, v79
	v_max3_f32 v80, v80, v77, v14
	v_max3_f32 v81, v81, v16, v17
	v_max3_f32 v80, v80, v15, v81
	v_mov_b32_e32 v81, v80
	s_nop 1
	v_permlane32_swap_b32_e32 v80, v81
	v_max_f32_e32 v81, v81, v81
	v_max_f32_e32 v80, v80, v80
	v_max_f32_e32 v80, v80, v81
	v_mul_f32_e32 v208, 0x3fb8aa3b, v80
	s_mov_b32 s27, 0
	s_mov_b32 s40, -1
	s_mov_b64 s[0:1], 0x8000
	s_mov_b64 s[28:29], 0x10000
	s_mov_b64 s[20:21], 0x18000
	s_mov_b64 s[8:9], 0x20000
	s_mov_b64 s[30:31], 0x28000
	s_mov_b64 s[14:15], 0x30000
	s_mov_b64 s[34:35], 0x38000
	v_fma_f32 v64, v64, s41, -v208
	v_fma_f32 v2, v2, s41, -v208
	v_fma_f32 v65, v65, s41, -v208
	v_fma_f32 v3, v3, s41, -v208
	v_fma_f32 v66, v66, s41, -v208
	v_fma_f32 v4, v4, s41, -v208
	v_fma_f32 v67, v67, s41, -v208
	v_fma_f32 v5, v5, s41, -v208
	v_fma_f32 v68, v68, s41, -v208
	v_fma_f32 v6, v6, s41, -v208
	v_fma_f32 v69, v69, s41, -v208
	v_fma_f32 v7, v7, s41, -v208
	v_fma_f32 v70, v70, s41, -v208
	v_fma_f32 v8, v8, s41, -v208
	v_fma_f32 v71, v71, s41, -v208
	v_fma_f32 v9, v9, s41, -v208
	v_fma_f32 v72, v72, s41, -v208
	v_fma_f32 v10, v10, s41, -v208
	v_fma_f32 v73, v73, s41, -v208
	v_fma_f32 v11, v11, s41, -v208
	v_fma_f32 v74, v74, s41, -v208
	v_fma_f32 v12, v12, s41, -v208
	v_fma_f32 v75, v75, s41, -v208
	v_fma_f32 v13, v13, s41, -v208
	v_fma_f32 v76, v76, s41, -v208
	v_fma_f32 v14, v14, s41, -v208
	v_fma_f32 v77, v77, s41, -v208
	v_fma_f32 v78, v78, s41, -v208
	v_fma_f32 v79, v79, s41, -v208
	v_fma_f32 v94, v15, s41, -v208
	v_fma_f32 v16, v16, s41, -v208
	v_fma_f32 v15, v17, s41, -v208
	s_and_b64 vcc, exec, s[4:5]
	s_cbranch_vccnz .LBB6_8
	v_lshl_add_u64 v[20:21], v[20:21], 0, s[14:15]
	s_mov_b32 m0, s39
	s_nop 0
	global_load_lds_dwordx4 v[20:21], off
.LBB6_8:
	v_lshl_add_u64 v[178:179], v[22:23], 0, s[0:1]
	s_and_b32 s0, s42, 0x3fffffc0
	s_lshl_b32 s0, s0, 2
	s_add_i32 s45, s0, 0
	s_add_i32 s0, s7, 0
	s_add_i32 s0, s0, 0x14800
	v_lshlrev_b32_e32 v0, 8, v0
	s_cmp_lg_u32 0, -1
	v_lshl_add_u64 v[170:171], v[22:23], 0, s[30:31]
	v_exp_f32_e32 v80, v64
	v_exp_f32_e32 v64, v2
	v_lshlrev_b32_e32 v2, 10, v104
	v_and_b32_e32 v0, 0x300, v0
	s_cselect_b32 s30, 0, 0
	v_add3_u32 v222, s0, v2, v0
	s_add_i32 s0, s30, s36
	s_add_i32 s44, s30, s7
	v_lshl_add_u64 v[166:167], v[26:27], 0, s[34:35]
	s_add_i32 s0, s0, 0x8000
	s_add_i32 s30, s44, 0x14c00
	s_add_i32 s31, s44, 0x15000
	s_add_i32 s34, s44, 0x15400
	s_add_i32 s35, s44, 0x15800
	s_add_i32 s42, s44, 0x15c00
	s_add_i32 s43, s44, 0x16000
	s_add_i32 s44, s44, 0x16400
	v_lshlrev_b32_e32 v0, 5, v28
	v_lshrrev_b32_e32 v2, 2, v31
	s_add_u32 s22, s6, s22
	v_and_b32_e32 v0, 32, v0
	v_or_b32_e32 v2, v29, v2
	s_addc_u32 s23, 0, s23
	s_lshl_b32 s2, s2, 4
	v_lshl_add_u64 v[174:175], v[26:27], 0, s[20:21]
	v_exp_f32_e32 v87, v71
	v_exp_f32_e32 v71, v9
	v_add_u32_e32 v0, 0, v0
	v_lshlrev_b32_e32 v2, 6, v2
	s_mov_b64 s[20:21], 0x40000
	v_add_u32_e32 v9, s3, v202
	s_and_b32 s2, s2, 0x780
	v_exp_f32_e32 v81, v65
	v_exp_f32_e32 v65, v3
	v_add3_u32 v207, v0, v30, v2
	v_lshl_add_u64 v[2:3], v[162:163], 0, s[20:21]
	s_mov_b32 m0, s0
	s_nop 0
	global_load_lds_dwordx4 v[2:3], off
	v_lshlrev_b32_e32 v184, 10, v9
	v_mov_b32_e32 v185, 0
	s_add_u32 s2, s26, s2
	ds_read_b128 v[112:115], v209 offset:8192
	ds_read_b128 v[104:107], v209 offset:10240
	ds_read_b128 v[116:119], v210 offset:8192
	ds_read_b128 v[108:111], v210 offset:10240
	v_cmp_gt_u32_e64 s[0:1], 32, v1
	v_lshl_add_u64 v[0:1], s[22:23], 0, v[184:185]
	s_addc_u32 s3, 0, 0
	v_lshl_add_u64 v[0:1], v[0:1], 0, v[18:19]
	s_add_u32 s2, s2, s24
	v_lshl_add_u64 v[0:1], s[10:11], 0, v[0:1]
	v_lshlrev_b32_e32 v184, 12, v9
	s_addc_u32 s3, s3, s25
	v_exp_f32_e32 v82, v66
	v_exp_f32_e32 v66, v4
	v_exp_f32_e32 v83, v67
	v_exp_f32_e32 v67, v5
	v_exp_f32_e32 v84, v68
	v_exp_f32_e32 v68, v6
	v_exp_f32_e32 v85, v69
	v_exp_f32_e32 v69, v7
	v_exp_f32_e32 v86, v70
	v_exp_f32_e32 v70, v8
	v_exp_f32_e32 v88, v72
	v_exp_f32_e32 v72, v10
	v_exp_f32_e32 v89, v73
	v_exp_f32_e32 v73, v11
	v_exp_f32_e32 v90, v74
	v_exp_f32_e32 v74, v12
	v_exp_f32_e32 v91, v75
	v_exp_f32_e32 v75, v13
	v_exp_f32_e32 v92, v76
	v_exp_f32_e32 v76, v14
	v_exp_f32_e32 v93, v77
	v_exp_f32_e32 v77, v94
	v_exp_f32_e32 v94, v78
	v_exp_f32_e32 v78, v16
	v_exp_f32_e32 v95, v79
	v_exp_f32_e32 v79, v15
	v_xor_b32_e32 v4, v204, v31
	v_lshl_add_u64 v[180:181], v[0:1], 0, s[28:29]
	v_lshl_add_u64 v[0:1], s[2:3], 0, v[184:185]
	v_mov_b32_e32 v161, v185
	s_waitcnt vmcnt(2) lgkmcnt(0)
	s_barrier
	v_lshlrev_b32_e32 v223, 4, v4
	v_lshl_add_u64 v[0:1], v[0:1], 0, v[160:161]
	v_xor_b32_e32 v2, 0x80, v223
	v_xor_b32_e32 v3, 32, v223
	v_xor_b32_e32 v4, 0xa0, v223
	v_xor_b32_e32 v5, 64, v223
	v_xor_b32_e32 v6, 0xc0, v223
	v_xor_b32_e32 v7, 0x60, v223
	v_xor_b32_e32 v8, 0xe0, v223
	v_lshl_add_u64 v[0:1], s[12:13], 0, v[0:1]
	v_lshl_add_u64 v[176:177], v[24:25], 0, s[28:29]
	v_lshl_add_u64 v[172:173], v[164:165], 0, s[8:9]
	v_lshl_add_u64 v[168:169], v[24:25], 0, s[14:15]
	v_lshl_add_u32 v206, v203, 2, s45
	v_lshl_add_u32 v205, v29, 2, s45
	v_lshl_add_u64 v[182:183], v[0:1], 0, s[20:21]
	s_movk_i32 s28, 0x4000
	s_movk_i32 s45, 0x2000
	s_mov_b64 s[2:3], 0
	s_mov_b32 s29, 0x41000000
	s_mov_b64 s[10:11], 0x300
	s_mov_b64 s[12:13], 0x80000
	s_mov_b64 s[22:23], 0x400
	v_add_u32_e32 v161, v222, v2
	v_add_u32_e32 v184, v222, v3
	v_add_u32_e32 v211, v222, v4
	v_add_u32_e32 v212, v222, v5
	v_add_u32_e32 v213, v222, v6
	v_add_u32_e32 v214, v222, v7
	v_add_u32_e32 v215, v222, v8
	v_mov_b32_e32 v0, v185
	v_mov_b32_e32 v1, v185
	v_mov_b32_e32 v2, v185
	v_mov_b32_e32 v3, v185
	v_mov_b32_e32 v4, v185
	v_mov_b32_e32 v5, v185
	v_mov_b32_e32 v6, v185
	v_mov_b32_e32 v7, v185
	v_mov_b32_e32 v8, v185
	v_mov_b32_e32 v9, v185
	v_mov_b32_e32 v10, v185
	v_mov_b32_e32 v11, v185
	v_mov_b32_e32 v12, v185
	v_mov_b32_e32 v13, v185
	v_mov_b32_e32 v14, v185
	v_mov_b32_e32 v15, v185
	v_mov_b32_e32 v16, v185
	v_mov_b32_e32 v17, v185
	v_mov_b32_e32 v18, v185
	v_mov_b32_e32 v19, v185
	v_mov_b32_e32 v20, v185
	v_mov_b32_e32 v21, v185
	v_mov_b32_e32 v22, v185
	v_mov_b32_e32 v23, v185
	v_mov_b32_e32 v24, v185
	v_mov_b32_e32 v25, v185
	v_mov_b32_e32 v26, v185
	v_mov_b32_e32 v27, v185
	v_mov_b32_e32 v28, v185
	v_mov_b32_e32 v29, v185
	v_mov_b32_e32 v30, v185
	v_mov_b32_e32 v31, v185
	v_add_u32_e32 v221, v222, v223
	ds_read_b128 v[48:51], v221
	ds_read_b128 v[32:35], v161
	ds_read_b128 v[52:55], v184
	ds_read_b128 v[36:39], v211
	ds_read_b128 v[56:59], v212
	ds_read_b128 v[40:43], v213
	ds_read_b128 v[60:63], v214
	ds_read_b128 v[44:47], v215
	s_waitcnt lgkmcnt(0)
	s_mov_b64 s[52:53], 0x200
	v_lshl_add_u64 v[224:225], v[164:165], 0, s[52:53]
	s_mov_b32 m0, s38
	s_nop 0
	global_load_lds_dwordx4 v[224:225], off nt
	v_lshl_add_u64 v[224:225], v[178:179], 0, s[52:53]
	s_mov_b32 m0, s30
	s_nop 0
	global_load_lds_dwordx4 v[224:225], off nt
	v_lshl_add_u64 v[224:225], v[176:177], 0, s[52:53]
	s_mov_b32 m0, s31
	s_nop 0
	global_load_lds_dwordx4 v[224:225], off nt
	v_lshl_add_u64 v[224:225], v[174:175], 0, s[52:53]
	s_mov_b32 m0, s34
	s_nop 0
	global_load_lds_dwordx4 v[224:225], off nt
	v_lshl_add_u64 v[224:225], v[172:173], 0, s[52:53]
	s_mov_b32 m0, s35
	s_nop 0
	global_load_lds_dwordx4 v[224:225], off nt
	v_lshl_add_u64 v[224:225], v[170:171], 0, s[52:53]
	s_mov_b32 m0, s42
	s_nop 0
	global_load_lds_dwordx4 v[224:225], off nt
	v_lshl_add_u64 v[224:225], v[168:169], 0, s[52:53]
	s_mov_b32 m0, s43
	s_nop 0
	global_load_lds_dwordx4 v[224:225], off nt
	v_lshl_add_u64 v[224:225], v[166:167], 0, s[52:53]
	s_mov_b32 m0, s44
	s_nop 0
	global_load_lds_dwordx4 v[224:225], off nt

	.amdhsa_kernel _Z6k_attnILi1024ELi2048ELi1024ELi1024ELi2048ELi1024ELb1ELb1EEvPKDF16_S1_S1_PKfPDF16_
		.amdhsa_group_segment_fixed_size 0
		.amdhsa_private_segment_fixed_size 0
		.amdhsa_kernarg_size 40
		.amdhsa_user_sgpr_count 2
		.amdhsa_user_sgpr_dispatch_ptr 0
		.amdhsa_user_sgpr_queue_ptr 0
		.amdhsa_user_sgpr_kernarg_segment_ptr 1
		.amdhsa_user_sgpr_dispatch_id 0
		.amdhsa_user_sgpr_kernarg_preload_length 0
		.amdhsa_user_sgpr_kernarg_preload_offset 0
		.amdhsa_user_sgpr_private_segment_size 0
		.amdhsa_uses_dynamic_stack 0
		.amdhsa_enable_private_segment 0
		.amdhsa_system_sgpr_workgroup_id_x 1
		.amdhsa_system_sgpr_workgroup_id_y 0
		.amdhsa_system_sgpr_workgroup_id_z 0
		.amdhsa_system_sgpr_workgroup_info 0
		.amdhsa_system_vgpr_workitem_id 0
		.amdhsa_next_free_vgpr 226
		.amdhsa_next_free_sgpr 54
		.amdhsa_accum_offset 228
		.amdhsa_reserve_vcc 1
		.amdhsa_float_round_mode_32 0
		.amdhsa_float_round_mode_16_64 0
		.amdhsa_float_denorm_mode_32 3
		.amdhsa_float_denorm_mode_16_64 3
		.amdhsa_dx10_clamp 1
		.amdhsa_ieee_mode 1
		.amdhsa_fp16_overflow 0
		.amdhsa_tg_split 0
		.amdhsa_exception_fp_ieee_invalid_op 0
		.amdhsa_exception_fp_denorm_src 0
		.amdhsa_exception_fp_ieee_div_zero 0
		.amdhsa_exception_fp_ieee_overflow 0
		.amdhsa_exception_fp_ieee_underflow 0
		.amdhsa_exception_fp_ieee_inexact 0
		.amdhsa_exception_int_div_zero 0
	.end_amdhsa_kernel

.LBB8_11:
	s_lshl_b32 s8, s17, 7
	s_or_b32 s8, s8, s19
	v_or_b32_e32 v85, s8, v74
	s_lshl_b32 s8, s15, 7
	s_or_b32 s8, s8, s18
	s_and_b64 vcc, exec, s[0:1]
	v_lshl_or_b32 v0, v1, 3, s8
	s_waitcnt vmcnt(0) lgkmcnt(0)
	s_barrier
	s_cbranch_vccnz .LBB8_21
	v_mov_b32_e32 v1, 0
	v_or_b32_e32 v66, 32, v85
	v_mad_i64_i32 v[76:77], s[0:1], v66, s10, v[0:1]
	v_lshl_add_u64 v[74:75], v[76:77], 1, s[2:3]
	global_load_dwordx4 v[68:71], v[74:75], off
	s_lshl_b32 s0, s11, 13
	v_lshl_add_u32 v66, v84, 4, 0
	v_add_u32_e32 v86, s0, v66
	ds_read_b128 v[78:81], v86
	ds_read_b128 v[88:91], v86 offset:1024
	s_cmp_lg_u64 s[6:7], 0
	s_cselect_b64 s[8:9], -1, 0
	v_lshl_add_u64 v[72:73], v[0:1], 2, s[6:7]
	s_waitcnt lgkmcnt(1)
	v_pk_add_f32 v[80:81], v[80:81], v[64:65]
	v_pk_add_f32 v[82:83], v[78:79], v[62:63]
	s_waitcnt lgkmcnt(0)
	v_pk_add_f32 v[78:79], v[90:91], v[60:61]
	ds_read_b128 v[64:67], v86 offset:2048
	ds_read_b128 v[60:63], v86 offset:3072
	v_pk_add_f32 v[58:59], v[88:89], v[58:59]
	s_and_b64 vcc, exec, s[8:9]
	s_cbranch_vccz .LBB8_14
	global_load_dwordx4 v[88:91], v[72:73], off
	global_load_dwordx4 v[92:95], v[72:73], off offset:16
	s_waitcnt vmcnt(1)
	v_pk_add_f32 v[80:81], v[80:81], v[90:91]
	v_pk_add_f32 v[82:83], v[82:83], v[88:89]
	s_waitcnt vmcnt(0)
	v_pk_add_f32 v[78:79], v[78:79], v[94:95]
	v_pk_add_f32 v[58:59], v[58:59], v[92:93]
.LBB8_14:
	s_waitcnt vmcnt(0)
	v_cvt_f32_f16_sdwa v89, v68 dst_sel:DWORD dst_unused:UNUSED_PAD src0_sel:WORD_1
	v_cvt_f32_f16_e32 v88, v68
	v_cvt_f32_f16_sdwa v91, v69 dst_sel:DWORD dst_unused:UNUSED_PAD src0_sel:WORD_1
	v_cvt_f32_f16_e32 v90, v69
	s_waitcnt lgkmcnt(0)
	v_pk_add_f32 v[52:53], v[62:63], v[52:53]
	v_pk_add_f32 v[68:69], v[82:83], v[88:89]
	v_cvt_f32_f16_sdwa v83, v70 dst_sel:DWORD dst_unused:UNUSED_PAD src0_sel:WORD_1
	v_cvt_f32_f16_e32 v82, v70
	v_cvt_f32_f16_sdwa v89, v71 dst_sel:DWORD dst_unused:UNUSED_PAD src0_sel:WORD_1
	v_cvt_f32_f16_e32 v88, v71
	v_pk_add_f32 v[80:81], v[80:81], v[90:91]
	v_pk_add_f32 v[58:59], v[58:59], v[82:83]
	v_cvt_pk_f16_f32 v68, v68, v69
	v_cvt_pk_f16_f32 v70, v58, v59
	v_pk_add_f32 v[58:59], v[78:79], v[88:89]
	v_cvt_pk_f16_f32 v69, v80, v81
	v_cvt_pk_f16_f32 v71, v58, v59
	v_lshl_add_u64 v[58:59], v[76:77], 1, s[4:5]
	global_store_dwordx4 v[58:59], v[68:71], off
	global_load_dwordx4 v[68:71], v[74:75], off offset:64
	v_cndmask_b32_e64 v62, 0, 1, s[8:9]
	v_pk_add_f32 v[56:57], v[66:67], v[56:57]
	v_pk_add_f32 v[54:55], v[64:65], v[54:55]
	v_cmp_ne_u32_e64 s[0:1], 1, v62
	s_andn2_b64 vcc, exec, s[8:9]
	v_pk_add_f32 v[50:51], v[60:61], v[50:51]
	s_cbranch_vccnz .LBB8_16
	global_load_dwordx4 v[60:63], v[72:73], off offset:128
	global_load_dwordx4 v[64:67], v[72:73], off offset:144
	s_waitcnt vmcnt(1)
	v_pk_add_f32 v[56:57], v[56:57], v[62:63]
	v_pk_add_f32 v[54:55], v[54:55], v[60:61]
	s_waitcnt vmcnt(0)
	v_pk_add_f32 v[52:53], v[52:53], v[66:67]
	v_pk_add_f32 v[50:51], v[50:51], v[64:65]
.LBB8_16:
	s_waitcnt vmcnt(0)
	v_cvt_f32_f16_sdwa v61, v68 dst_sel:DWORD dst_unused:UNUSED_PAD src0_sel:WORD_1
	v_cvt_f32_f16_e32 v60, v68
	v_cvt_f32_f16_sdwa v63, v69 dst_sel:DWORD dst_unused:UNUSED_PAD src0_sel:WORD_1
	v_cvt_f32_f16_e32 v62, v69
	v_or_b32_e32 v74, 48, v85
	v_pk_add_f32 v[54:55], v[54:55], v[60:61]
	v_cvt_f32_f16_sdwa v61, v70 dst_sel:DWORD dst_unused:UNUSED_PAD src0_sel:WORD_1
	v_cvt_f32_f16_e32 v60, v70
	v_pk_add_f32 v[56:57], v[56:57], v[62:63]
	v_cvt_f32_f16_sdwa v63, v71 dst_sel:DWORD dst_unused:UNUSED_PAD src0_sel:WORD_1
	v_cvt_f32_f16_e32 v62, v71
	v_pk_add_f32 v[50:51], v[50:51], v[60:61]
	v_cvt_pk_f16_f32 v54, v54, v55
	v_cvt_pk_f16_f32 v55, v56, v57
	v_cvt_pk_f16_f32 v56, v50, v51
	v_pk_add_f32 v[50:51], v[52:53], v[62:63]
	v_mad_i64_i32 v[60:61], s[8:9], v74, s10, v[0:1]
	v_cvt_pk_f16_f32 v57, v50, v51
	global_store_dwordx4 v[58:59], v[54:57], off offset:64
	v_lshl_add_u64 v[58:59], v[60:61], 1, s[2:3]
	global_load_dwordx4 v[50:53], v[58:59], off
	ds_read_b128 v[54:57], v86 offset:4096
	ds_read_b128 v[68:71], v86 offset:5120
	s_and_b64 vcc, exec, s[0:1]
	s_waitcnt lgkmcnt(1)
	v_pk_add_f32 v[64:65], v[56:57], v[48:49]
	v_pk_add_f32 v[66:67], v[54:55], v[46:47]
	s_waitcnt lgkmcnt(0)
	v_pk_add_f32 v[62:63], v[70:71], v[44:45]
	ds_read_b128 v[54:57], v86 offset:6144
	ds_read_b128 v[44:47], v86 offset:7168
	v_pk_add_f32 v[42:43], v[68:69], v[42:43]
	v_mad_i64_i32 v[48:49], s[8:9], v74, s10, 0
	s_cbranch_vccnz .LBB8_18
	global_load_dwordx4 v[68:71], v[72:73], off
	global_load_dwordx4 v[74:77], v[72:73], off offset:16
	s_waitcnt vmcnt(1)
	v_pk_add_f32 v[64:65], v[64:65], v[70:71]
	v_pk_add_f32 v[66:67], v[66:67], v[68:69]
	s_waitcnt vmcnt(0)
	v_pk_add_f32 v[62:63], v[62:63], v[76:77]
	v_pk_add_f32 v[42:43], v[42:43], v[74:75]
.LBB8_18:
	s_waitcnt lgkmcnt(0)
	v_pk_add_f32 v[34:35], v[44:45], v[34:35]
	s_waitcnt vmcnt(0)
	v_cvt_f32_f16_sdwa v45, v50 dst_sel:DWORD dst_unused:UNUSED_PAD src0_sel:WORD_1
	v_cvt_f32_f16_e32 v44, v50
	v_pk_add_f32 v[38:39], v[54:55], v[38:39]
	v_cvt_f32_f16_sdwa v55, v51 dst_sel:DWORD dst_unused:UNUSED_PAD src0_sel:WORD_1
	v_cvt_f32_f16_e32 v54, v51
	v_pk_add_f32 v[44:45], v[66:67], v[44:45]
	v_pk_add_f32 v[40:41], v[56:57], v[40:41]
	v_cvt_pk_f16_f32 v50, v44, v45
	v_pk_add_f32 v[44:45], v[64:65], v[54:55]
	v_cvt_f32_f16_sdwa v55, v52 dst_sel:DWORD dst_unused:UNUSED_PAD src0_sel:WORD_1
	v_cvt_f32_f16_e32 v54, v52
	v_cvt_f32_f16_sdwa v57, v53 dst_sel:DWORD dst_unused:UNUSED_PAD src0_sel:WORD_1
	v_cvt_f32_f16_e32 v56, v53
	v_pk_add_f32 v[36:37], v[46:47], v[36:37]
	v_pk_add_f32 v[42:43], v[42:43], v[54:55]
	v_or_b32_e32 v46, 32, v0
	v_cvt_pk_f16_f32 v52, v42, v43
	v_pk_add_f32 v[42:43], v[62:63], v[56:57]
	v_mov_b32_e32 v47, 0
	v_cvt_pk_f16_f32 v51, v44, v45
	v_cvt_pk_f16_f32 v53, v42, v43
	v_lshl_add_u64 v[42:43], v[60:61], 1, s[4:5]
	s_and_b64 vcc, exec, s[0:1]
	global_store_dwordx4 v[42:43], v[50:53], off
	s_cbranch_vccnz .LBB8_20
	global_load_dwordx4 v[42:45], v[72:73], off offset:128
	global_load_dwordx4 v[50:53], v[72:73], off offset:144
	s_waitcnt vmcnt(1)
	v_pk_add_f32 v[40:41], v[40:41], v[44:45]
	v_pk_add_f32 v[38:39], v[38:39], v[42:43]
	s_waitcnt vmcnt(0)
	v_pk_add_f32 v[36:37], v[36:37], v[52:53]
	v_pk_add_f32 v[34:35], v[34:35], v[50:51]
.LBB8_20:
	global_load_dwordx4 v[42:45], v[58:59], off offset:64
	v_lshl_add_u64 v[46:47], v[48:49], 0, v[46:47]
	s_branch .LBB8_31
.LBB8_21:
	s_cbranch_execz .LBB8_31
	v_mov_b32_e32 v1, 0
	v_mad_i64_i32 v[50:51], s[0:1], v85, s10, v[0:1]
	v_lshl_add_u64 v[48:49], v[50:51], 1, s[2:3]
	global_load_dwordx4 v[42:45], v[48:49], off
	s_cmp_lg_u64 s[6:7], 0
	s_cselect_b64 s[8:9], -1, 0
	s_lshl_b32 s0, s14, 13
	s_add_i32 s0, s0, 0
	v_lshl_add_u32 v56, v84, 4, s0
	ds_read_b128 v[58:61], v56 offset:32768
	ds_read_b128 v[62:65], v56 offset:33792
	ds_read_b128 v[38:41], v56 offset:34816
	ds_read_b128 v[34:37], v56 offset:35840
	s_cmp_eq_u64 s[6:7], 0
	v_lshl_add_u64 v[46:47], v[0:1], 2, s[6:7]
	s_waitcnt lgkmcnt(3)
	v_pk_add_f32 v[52:53], v[60:61], v[28:29]
	v_pk_add_f32 v[54:55], v[58:59], v[26:27]
	s_waitcnt lgkmcnt(2)
	v_pk_add_f32 v[26:27], v[64:65], v[32:33]
	v_pk_add_f32 v[28:29], v[62:63], v[30:31]
	s_cbranch_scc1 .LBB8_24
	global_load_dwordx4 v[30:33], v[46:47], off
	global_load_dwordx4 v[58:61], v[46:47], off offset:16
	s_waitcnt vmcnt(1)
	v_pk_add_f32 v[52:53], v[52:53], v[32:33]
	v_pk_add_f32 v[54:55], v[54:55], v[30:31]
	s_waitcnt vmcnt(0)
	v_pk_add_f32 v[26:27], v[26:27], v[60:61]
	v_pk_add_f32 v[28:29], v[28:29], v[58:59]
.LBB8_24:
	s_waitcnt vmcnt(0)
	v_cvt_f32_f16_sdwa v31, v42 dst_sel:DWORD dst_unused:UNUSED_PAD src0_sel:WORD_1
	v_cvt_f32_f16_e32 v30, v42
	v_cvt_f32_f16_sdwa v33, v43 dst_sel:DWORD dst_unused:UNUSED_PAD src0_sel:WORD_1
	v_cvt_f32_f16_e32 v32, v43
	s_waitcnt lgkmcnt(1)
	v_pk_add_f32 v[24:25], v[40:41], v[24:25]
	v_pk_add_f32 v[30:31], v[54:55], v[30:31]
	v_pk_add_f32 v[22:23], v[38:39], v[22:23]
	v_cvt_pk_f16_f32 v42, v30, v31
	v_pk_add_f32 v[30:31], v[52:53], v[32:33]
	v_cvt_f32_f16_sdwa v33, v44 dst_sel:DWORD dst_unused:UNUSED_PAD src0_sel:WORD_1
	v_cvt_f32_f16_e32 v32, v44
	v_cvt_f32_f16_sdwa v53, v45 dst_sel:DWORD dst_unused:UNUSED_PAD src0_sel:WORD_1
	v_cvt_f32_f16_e32 v52, v45
	v_cvt_pk_f16_f32 v43, v30, v31
	v_pk_add_f32 v[28:29], v[28:29], v[32:33]
	v_lshl_add_u64 v[30:31], v[50:51], 1, s[4:5]
	v_pk_add_f32 v[26:27], v[26:27], v[52:53]
	v_cvt_pk_f16_f32 v44, v28, v29
	v_cvt_pk_f16_f32 v45, v26, v27
	global_store_dwordx4 v[30:31], v[42:45], off
	global_load_dwordx4 v[26:29], v[48:49], off offset:64
	v_cndmask_b32_e64 v32, 0, 1, s[8:9]
	s_waitcnt lgkmcnt(0)
	v_pk_add_f32 v[20:21], v[36:37], v[20:21]
	v_cmp_ne_u32_e64 s[0:1], 1, v32
	s_andn2_b64 vcc, exec, s[8:9]
	v_pk_add_f32 v[18:19], v[34:35], v[18:19]
	s_cbranch_vccnz .LBB8_26
	global_load_dwordx4 v[32:35], v[46:47], off offset:128
	global_load_dwordx4 v[36:39], v[46:47], off offset:144
	s_waitcnt vmcnt(1)
	v_pk_add_f32 v[24:25], v[24:25], v[34:35]
	v_pk_add_f32 v[22:23], v[22:23], v[32:33]
	s_waitcnt vmcnt(0)
	v_pk_add_f32 v[20:21], v[20:21], v[38:39]
	v_pk_add_f32 v[18:19], v[18:19], v[36:37]
.LBB8_26:
	s_waitcnt vmcnt(0)
	v_cvt_f32_f16_sdwa v33, v26 dst_sel:DWORD dst_unused:UNUSED_PAD src0_sel:WORD_1
	v_cvt_f32_f16_e32 v32, v26
	v_cvt_f32_f16_sdwa v35, v27 dst_sel:DWORD dst_unused:UNUSED_PAD src0_sel:WORD_1
	v_cvt_f32_f16_e32 v34, v27
	v_cvt_f32_f16_sdwa v27, v28 dst_sel:DWORD dst_unused:UNUSED_PAD src0_sel:WORD_1
	v_cvt_f32_f16_e32 v26, v28
	v_pk_add_f32 v[22:23], v[22:23], v[32:33]
	v_cvt_f32_f16_sdwa v33, v29 dst_sel:DWORD dst_unused:UNUSED_PAD src0_sel:WORD_1
	v_cvt_f32_f16_e32 v32, v29
	v_pk_add_f32 v[24:25], v[24:25], v[34:35]
	v_pk_add_f32 v[18:19], v[18:19], v[26:27]
	v_cvt_pk_f16_f32 v22, v22, v23
	v_cvt_pk_f16_f32 v23, v24, v25
	v_cvt_pk_f16_f32 v24, v18, v19
	v_pk_add_f32 v[18:19], v[20:21], v[32:33]
	v_or_b32_e32 v38, 16, v85
	v_cvt_pk_f16_f32 v25, v18, v19
	v_mad_i64_i32 v[28:29], s[6:7], v38, s10, v[0:1]
	global_store_dwordx4 v[30:31], v[22:25], off offset:64
	v_lshl_add_u64 v[26:27], v[28:29], 1, s[2:3]
	global_load_dwordx4 v[18:21], v[26:27], off
	ds_read_b128 v[22:25], v56 offset:36864
	ds_read_b128 v[34:37], v56 offset:37888
	s_and_b64 vcc, exec, s[0:1]
	s_waitcnt lgkmcnt(1)
	v_pk_add_f32 v[32:33], v[24:25], v[16:17]
	v_pk_add_f32 v[42:43], v[22:23], v[14:15]
	s_waitcnt lgkmcnt(0)
	v_pk_add_f32 v[16:17], v[36:37], v[12:13]
	ds_read_b128 v[22:25], v56 offset:38912
	ds_read_b128 v[12:15], v56 offset:39936
	v_pk_add_f32 v[30:31], v[34:35], v[10:11]
	v_mad_i64_i32 v[10:11], s[2:3], v38, s10, 0
	s_cbranch_vccnz .LBB8_28
	global_load_dwordx4 v[34:37], v[46:47], off
	global_load_dwordx4 v[38:41], v[46:47], off offset:16
	s_waitcnt vmcnt(1)
	v_pk_add_f32 v[32:33], v[32:33], v[36:37]
	v_pk_add_f32 v[42:43], v[42:43], v[34:35]
	s_waitcnt vmcnt(0)
	v_pk_add_f32 v[16:17], v[16:17], v[40:41]
	v_pk_add_f32 v[30:31], v[30:31], v[38:39]
.LBB8_28:
	s_waitcnt lgkmcnt(0)
	v_pk_add_f32 v[36:37], v[14:15], v[4:5]
	v_pk_add_f32 v[34:35], v[12:13], v[2:3]
	s_waitcnt vmcnt(0)
	v_cvt_f32_f16_sdwa v3, v18 dst_sel:DWORD dst_unused:UNUSED_PAD src0_sel:WORD_1
	v_cvt_f32_f16_e32 v2, v18
	v_cvt_f32_f16_sdwa v5, v19 dst_sel:DWORD dst_unused:UNUSED_PAD src0_sel:WORD_1
	v_cvt_f32_f16_e32 v4, v19
	v_pk_add_f32 v[40:41], v[24:25], v[8:9]
	v_pk_add_f32 v[38:39], v[22:23], v[6:7]
	v_cvt_f32_f16_sdwa v7, v20 dst_sel:DWORD dst_unused:UNUSED_PAD src0_sel:WORD_1
	v_cvt_f32_f16_e32 v6, v20
	v_cvt_f32_f16_sdwa v9, v21 dst_sel:DWORD dst_unused:UNUSED_PAD src0_sel:WORD_1
	v_cvt_f32_f16_e32 v8, v21
	v_pk_add_f32 v[2:3], v[42:43], v[2:3]
	v_pk_add_f32 v[4:5], v[32:33], v[4:5]
	v_cvt_pk_f16_f32 v2, v2, v3
	v_cvt_pk_f16_f32 v3, v4, v5
	v_pk_add_f32 v[4:5], v[30:31], v[6:7]
	v_pk_add_f32 v[6:7], v[16:17], v[8:9]
	v_or_b32_e32 v0, 32, v0
	v_mov_b32_e32 v1, 0
	v_cvt_pk_f16_f32 v4, v4, v5
	v_cvt_pk_f16_f32 v5, v6, v7
	v_lshl_add_u64 v[6:7], v[28:29], 1, s[4:5]
	s_and_b64 vcc, exec, s[0:1]
	global_store_dwordx4 v[6:7], v[2:5], off
	s_cbranch_vccnz .LBB8_30
	global_load_dwordx4 v[2:5], v[46:47], off offset:128
	global_load_dwordx4 v[6:9], v[46:47], off offset:144
	s_waitcnt vmcnt(1)
	v_pk_add_f32 v[40:41], v[40:41], v[4:5]
	v_pk_add_f32 v[38:39], v[38:39], v[2:3]
	s_waitcnt vmcnt(0)
	v_pk_add_f32 v[36:37], v[36:37], v[8:9]
	v_pk_add_f32 v[34:35], v[34:35], v[6:7]
.LBB8_30:
	global_load_dwordx4 v[42:45], v[26:27], off offset:64
	v_lshl_add_u64 v[46:47], v[10:11], 0, v[0:1]
.LBB8_31:
	s_waitcnt vmcnt(0)
	v_cvt_f32_f16_sdwa v1, v42 dst_sel:DWORD dst_unused:UNUSED_PAD src0_sel:WORD_1
	v_cvt_f32_f16_e32 v0, v42
	v_cvt_f32_f16_sdwa v3, v43 dst_sel:DWORD dst_unused:UNUSED_PAD src0_sel:WORD_1
	v_cvt_f32_f16_e32 v2, v43
	v_cvt_f32_f16_sdwa v5, v44 dst_sel:DWORD dst_unused:UNUSED_PAD src0_sel:WORD_1
	v_cvt_f32_f16_e32 v4, v44
	v_cvt_f32_f16_sdwa v7, v45 dst_sel:DWORD dst_unused:UNUSED_PAD src0_sel:WORD_1
	v_cvt_f32_f16_e32 v6, v45
	v_pk_add_f32 v[0:1], v[38:39], v[0:1]
	v_pk_add_f32 v[2:3], v[40:41], v[2:3]
	v_cvt_pk_f16_f32 v0, v0, v1
	v_cvt_pk_f16_f32 v1, v2, v3
	v_pk_add_f32 v[2:3], v[34:35], v[4:5]
	v_pk_add_f32 v[4:5], v[36:37], v[6:7]
	v_cvt_pk_f16_f32 v2, v2, v3
	v_cvt_pk_f16_f32 v3, v4, v5
	v_lshl_add_u64 v[4:5], v[46:47], 1, s[4:5]
	global_store_dwordx4 v[4:5], v[0:3], off
	s_endpgm
	.p2align	8

	.amdhsa_kernel _ZN4g1289k_gemm128INS_8EpiRes16EEEvPKDF16_S3_iiiT_
		.amdhsa_group_segment_fixed_size 0
		.amdhsa_private_segment_fixed_size 0
		.amdhsa_kernarg_size 64
		.amdhsa_user_sgpr_count 2
		.amdhsa_user_sgpr_dispatch_ptr 0
		.amdhsa_user_sgpr_queue_ptr 0
		.amdhsa_user_sgpr_kernarg_segment_ptr 1
		.amdhsa_user_sgpr_dispatch_id 0
		.amdhsa_user_sgpr_kernarg_preload_length 0
		.amdhsa_user_sgpr_kernarg_preload_offset 0
		.amdhsa_user_sgpr_private_segment_size 0
		.amdhsa_uses_dynamic_stack 0
		.amdhsa_enable_private_segment 0
		.amdhsa_system_sgpr_workgroup_id_x 1
		.amdhsa_system_sgpr_workgroup_id_y 0
		.amdhsa_system_sgpr_workgroup_id_z 0
		.amdhsa_system_sgpr_workgroup_info 0
		.amdhsa_system_vgpr_workitem_id 0
		.amdhsa_next_free_vgpr 112
		.amdhsa_next_free_sgpr 29
		.amdhsa_accum_offset 112
		.amdhsa_reserve_vcc 1
		.amdhsa_float_round_mode_32 0
		.amdhsa_float_round_mode_16_64 0
		.amdhsa_float_denorm_mode_32 3
		.amdhsa_float_denorm_mode_16_64 3
		.amdhsa_dx10_clamp 1
		.amdhsa_ieee_mode 1
		.amdhsa_fp16_overflow 0
		.amdhsa_tg_split 0
		.amdhsa_exception_fp_ieee_invalid_op 0
		.amdhsa_exception_fp_denorm_src 0
		.amdhsa_exception_fp_ieee_div_zero 0
		.amdhsa_exception_fp_ieee_overflow 0
		.amdhsa_exception_fp_ieee_underflow 0
		.amdhsa_exception_fp_ieee_inexact 0
		.amdhsa_exception_int_div_zero 0
	.end_amdhsa_kernel

amdhsa.kernels:
  - .agpr_count:     0
    .args:
      - .offset:         0
        .size:           384
        .value_kind:     by_value
    .group_segment_fixed_size: 5120
    .kernarg_segment_align: 8
    .kernarg_segment_size: 384
    .language:       OpenCL C
    .language_version:
      - 2
      - 0
    .max_flat_workgroup_size: 256
    .name:           _Z6k_prep6WtArgs
    .private_segment_fixed_size: 0
    .sgpr_count:     38
    .sgpr_spill_count: 0
    .symbol:         _Z6k_prep6WtArgs.kd
    .uniform_work_group_size: 1
    .uses_dynamic_stack: false
    .vgpr_count:     29
    .vgpr_spill_count: 0
    .wavefront_size: 64
  - .agpr_count:     0
    .args:
      - .actual_access:  read_only
        .address_space:  global
        .offset:         0
        .size:           8
        .value_kind:     global_buffer
      - .actual_access:  read_only
        .address_space:  global
        .offset:         8
        .size:           8
        .value_kind:     global_buffer
      - .actual_access:  read_only
        .address_space:  global
        .offset:         16
        .size:           8
        .value_kind:     global_buffer
      - .actual_access:  write_only
        .address_space:  global
        .offset:         24
        .size:           8
        .value_kind:     global_buffer
      - .actual_access:  write_only
        .address_space:  global
        .offset:         32
        .size:           8
        .value_kind:     global_buffer
      - .actual_access:  write_only
        .address_space:  global
        .offset:         40
        .size:           8
        .value_kind:     global_buffer
      - .offset:         48
        .size:           4
        .value_kind:     by_value
    .group_segment_fixed_size: 0
    .kernarg_segment_align: 8
    .kernarg_segment_size: 52
    .language:       OpenCL C
    .language_version:
      - 2
      - 0
    .max_flat_workgroup_size: 256
    .name:           _Z4k_lnPKDF16_PKfS2_PfPDF16_Phi
    .private_segment_fixed_size: 0
    .sgpr_count:     18
    .sgpr_spill_count: 0
    .symbol:         _Z4k_lnPKDF16_PKfS2_PfPDF16_Phi.kd
    .uniform_work_group_size: 1
    .uses_dynamic_stack: false
    .vgpr_count:     59
    .vgpr_spill_count: 0
    .wavefront_size: 64
  - .agpr_count:     0
    .args:
      - .offset:         0
        .size:           56
        .value_kind:     by_value
      - .offset:         56
        .size:           72
        .value_kind:     by_value
      - .offset:         128
        .size:           176
        .value_kind:     by_value
      - .address_space:  global
        .offset:         304
        .size:           8
        .value_kind:     global_buffer
      - .offset:         312
        .size:           4
        .value_kind:     hidden_block_count_x
      - .offset:         316
        .size:           4
        .value_kind:     hidden_block_count_y
      - .offset:         320
        .size:           4
        .value_kind:     hidden_block_count_z
      - .offset:         324
        .size:           2
        .value_kind:     hidden_group_size_x
      - .offset:         326
        .size:           2
        .value_kind:     hidden_group_size_y
      - .offset:         328
        .size:           2
        .value_kind:     hidden_group_size_z
      - .offset:         330
        .size:           2
        .value_kind:     hidden_remainder_x
      - .offset:         332
        .size:           2
        .value_kind:     hidden_remainder_y
      - .offset:         334
        .size:           2
        .value_kind:     hidden_remainder_z
      - .offset:         352
        .size:           8
        .value_kind:     hidden_global_offset_x
      - .offset:         360
        .size:           8
        .value_kind:     hidden_global_offset_y
      - .offset:         368
        .size:           8
        .value_kind:     hidden_global_offset_z
      - .offset:         376
        .size:           2
        .value_kind:     hidden_grid_dims
      - .offset:         432
        .size:           4
        .value_kind:     hidden_dynamic_lds_size
    .group_segment_fixed_size: 0
    .kernarg_segment_align: 8
    .kernarg_segment_size: 568
    .language:       OpenCL C
    .language_version:
      - 2
      - 0
    .max_flat_workgroup_size: 512
    .name:           _Z6k_gemmIN3pg84EpiHILi0ELb1EEELb1EEvNS0_4GemmET_6WtTailPj
    .private_segment_fixed_size: 0
    .sgpr_count:     60
    .sgpr_spill_count: 5
    .symbol:         _Z6k_gemmIN3pg84EpiHILi0ELb1EEELb1EEvNS0_4GemmET_6WtTailPj.kd
    .uniform_work_group_size: 1
    .uses_dynamic_stack: false
    .vgpr_count:     226
    .vgpr_spill_count: 0
    .wavefront_size: 64
  - .agpr_count:     0
    .args:
      - .address_space:  global
        .offset:         0
        .size:           8
        .value_kind:     global_buffer
      - .address_space:  global
        .offset:         8
        .size:           8
        .value_kind:     global_buffer
      - .address_space:  global
        .offset:         16
        .size:           8
        .value_kind:     global_buffer
      - .address_space:  global
        .offset:         24
        .size:           8
        .value_kind:     global_buffer
      - .address_space:  global
        .offset:         32
        .size:           8
        .value_kind:     global_buffer
    .group_segment_fixed_size: 0
    .kernarg_segment_align: 8
    .kernarg_segment_size: 40
    .language:       OpenCL C
    .language_version:
      - 2
      - 0
    .max_flat_workgroup_size: 512
    .name:           _Z6k_attnILi1024ELi1024ELi1024ELi1024ELi3072ELi1024ELb1ELb1EEvPKDF16_S1_S1_PKfPDF16_
    .private_segment_fixed_size: 0
    .sgpr_count:     55
    .sgpr_spill_count: 0
    .symbol:         _Z6k_attnILi1024ELi1024ELi1024ELi1024ELi3072ELi1024ELb1ELb1EEvPKDF16_S1_S1_PKfPDF16_.kd
    .uniform_work_group_size: 1
    .uses_dynamic_stack: false
    .vgpr_count:     224
    .vgpr_spill_count: 0
    .wavefront_size: 64
  - .agpr_count:     0
    .args:
      - .address_space:  global
        .offset:         0
        .size:           8
        .value_kind:     global_buffer
      - .address_space:  global
        .offset:         8
        .size:           8
        .value_kind:     global_buffer
      - .offset:         16
        .size:           4
        .value_kind:     by_value
      - .offset:         20
        .size:           4
        .value_kind:     by_value
      - .offset:         24
        .size:           4
        .value_kind:     by_value
      - .offset:         32
        .size:           32
        .value_kind:     by_value
    .group_segment_fixed_size: 0
    .kernarg_segment_align: 8
    .kernarg_segment_size: 64
    .language:       OpenCL C
    .language_version:
      - 2
      - 0
    .max_flat_workgroup_size: 512
    .name:           _ZN2g811k_gemm128f8INS_6EpiResEEEvPKhS3_iiiT_
    .private_segment_fixed_size: 0
    .sgpr_count:     34
    .sgpr_spill_count: 0
    .symbol:         _ZN2g811k_gemm128f8INS_6EpiResEEEvPKhS3_iiiT_.kd
    .uniform_work_group_size: 1
    .uses_dynamic_stack: false
    .vgpr_count:     98
    .vgpr_spill_count: 0
    .wavefront_size: 64
  - .agpr_count:     0
    .args:
      - .address_space:  global
        .offset:         0
        .size:           8
        .value_kind:     global_buffer
      - .address_space:  global
        .offset:         8
        .size:           8
        .value_kind:     global_buffer
      - .offset:         16
        .size:           4
        .value_kind:     by_value
      - .offset:         20
        .size:           4
        .value_kind:     by_value
      - .offset:         24
        .size:           4
        .value_kind:     by_value
      - .offset:         32
        .size:           16
        .value_kind:     by_value
    .group_segment_fixed_size: 0
    .kernarg_segment_align: 8
    .kernarg_segment_size: 48
    .language:       OpenCL C
    .language_version:
      - 2
      - 0
    .max_flat_workgroup_size: 512
    .name:           _ZN2g811k_gemm128f8INS_5EpiQ8EEEvPKhS3_iiiT_
    .private_segment_fixed_size: 0
    .sgpr_count:     60
    .sgpr_spill_count: 0
    .symbol:         _ZN2g811k_gemm128f8INS_5EpiQ8EEEvPKhS3_iiiT_.kd
    .uniform_work_group_size: 1
    .uses_dynamic_stack: false
    .vgpr_count:     226
    .vgpr_spill_count: 0
    .wavefront_size: 64
  - .agpr_count:     0
    .args:
      - .address_space:  global
        .offset:         0
        .size:           8
        .value_kind:     global_buffer
      - .address_space:  global
        .offset:         8
        .size:           8
        .value_kind:     global_buffer
      - .address_space:  global
        .offset:         16
        .size:           8
        .value_kind:     global_buffer
      - .address_space:  global
        .offset:         24
        .size:           8
        .value_kind:     global_buffer
      - .address_space:  global
        .offset:         32
        .size:           8
        .value_kind:     global_buffer
    .group_segment_fixed_size: 0
    .kernarg_segment_align: 8
    .kernarg_segment_size: 40
    .language:       OpenCL C
    .language_version:
      - 2
      - 0
    .max_flat_workgroup_size: 512
    .name:           _Z6k_attnILi1024ELi2048ELi1024ELi1024ELi2048ELi1024ELb1ELb1EEvPKDF16_S1_S1_PKfPDF16_
    .private_segment_fixed_size: 0
    .sgpr_count:     52
    .sgpr_spill_count: 0
    .symbol:         _Z6k_attnILi1024ELi2048ELi1024ELi1024ELi2048ELi1024ELb1ELb1EEvPKDF16_S1_S1_PKfPDF16_.kd
    .uniform_work_group_size: 1
    .uses_dynamic_stack: false
    .vgpr_count:     224
    .vgpr_spill_count: 0
    .wavefront_size: 64
  - .agpr_count:     0
    .args:
      - .offset:         0
        .size:           56
        .value_kind:     by_value
      - .offset:         56
        .size:           72
        .value_kind:     by_value
      - .offset:         128
        .size:           176
        .value_kind:     by_value
      - .address_space:  global
        .offset:         304
        .size:           8
        .value_kind:     global_buffer
      - .offset:         312
        .size:           4
        .value_kind:     hidden_block_count_x
      - .offset:         316
        .size:           4
        .value_kind:     hidden_block_count_y
      - .offset:         320
        .size:           4
        .value_kind:     hidden_block_count_z
      - .offset:         324
        .size:           2
        .value_kind:     hidden_group_size_x
      - .offset:         326
        .size:           2
        .value_kind:     hidden_group_size_y
      - .offset:         328
        .size:           2
        .value_kind:     hidden_group_size_z
      - .offset:         330
        .size:           2
        .value_kind:     hidden_remainder_x
      - .offset:         332
        .size:           2
        .value_kind:     hidden_remainder_y
      - .offset:         334
        .size:           2
        .value_kind:     hidden_remainder_z
      - .offset:         352
        .size:           8
        .value_kind:     hidden_global_offset_x
      - .offset:         360
        .size:           8
        .value_kind:     hidden_global_offset_y
      - .offset:         368
        .size:           8
        .value_kind:     hidden_global_offset_z
      - .offset:         376
        .size:           2
        .value_kind:     hidden_grid_dims
      - .offset:         432
        .size:           4
        .value_kind:     hidden_dynamic_lds_size
    .group_segment_fixed_size: 0
    .kernarg_segment_align: 8
    .kernarg_segment_size: 568
    .language:       OpenCL C
    .language_version:
      - 2
      - 0
    .max_flat_workgroup_size: 512
    .name:           _Z6k_gemmIN3pg84EpiHILi1ELb0EEELb0EEvNS0_4GemmET_6WtTailPj
    .private_segment_fixed_size: 0
    .sgpr_count:     85
    .sgpr_spill_count: 0
    .symbol:         _Z6k_gemmIN3pg84EpiHILi1ELb0EEELb0EEvNS0_4GemmET_6WtTailPj.kd
    .uniform_work_group_size: 1
    .uses_dynamic_stack: false
    .vgpr_count:     242
    .vgpr_spill_count: 0
    .wavefront_size: 64
  - .agpr_count:     0
    .args:
      - .address_space:  global
        .offset:         0
        .size:           8
        .value_kind:     global_buffer
      - .address_space:  global
        .offset:         8
        .size:           8
        .value_kind:     global_buffer
      - .offset:         16
        .size:           4
        .value_kind:     by_value
      - .offset:         20
        .size:           4
        .value_kind:     by_value
      - .offset:         24
        .size:           4
        .value_kind:     by_value
      - .offset:         32
        .size:           32
        .value_kind:     by_value
    .group_segment_fixed_size: 0
    .kernarg_segment_align: 8
    .kernarg_segment_size: 64
    .language:       OpenCL C
    .language_version:
      - 2
      - 0
    .max_flat_workgroup_size: 512
    .name:           _ZN4g1289k_gemm128INS_8EpiRes16EEEvPKDF16_S3_iiiT_
    .private_segment_fixed_size: 0
    .sgpr_count:     35
    .sgpr_spill_count: 0
    .symbol:         _ZN4g1289k_gemm128INS_8EpiRes16EEEvPKDF16_S3_iiiT_.kd
    .uniform_work_group_size: 1
    .uses_dynamic_stack: false
    .vgpr_count:     112
    .vgpr_spill_count: 0
    .wavefront_size: 64
